# GEMM K-loops: 12 of the 16 LDS-DMA staging loads per loop body in scalar-base form, their 64-bit VALU address adds dropped
# speedup vs baseline: 1.0228x; 1.0228x over previous
.LBB0_119:
	ds_read_b128 v[148:151], v153
	ds_read_b128 v[156:159], v153 offset:1024
	ds_read_b128 v[160:163], v153 offset:2048
	ds_read_b128 v[164:167], v153 offset:3072
	ds_read_b128 v[168:171], v154
	ds_read_b128 v[172:175], v154 offset:1024
	ds_read_b128 v[176:179], v154 offset:2048
	ds_read_b128 v[180:183], v154 offset:3072
	s_add_u32 s24, s22, 0xfff80080
	s_addc_u32 s25, s23, -1
	s_cmp_eq_u32 s79, 28
	s_cselect_b32 s27, s15, s25
	s_cselect_b32 s26, s75, s24
	s_cselect_b32 s25, s13, s78
	s_cselect_b32 s24, s76, s77
	s_add_i32 m0, s21, 0xc000
	ds_read_b128 v[184:187], v155
	ds_read_b128 v[188:191], v155 offset:1024
	ds_read_b128 v[192:195], v155 offset:2048
	ds_read_b128 v[196:199], v155 offset:3072
	ds_read_b128 v[200:203], v155 offset:4096
	ds_read_b128 v[204:207], v155 offset:5120
	ds_read_b128 v[208:211], v155 offset:6144
	ds_read_b128 v[212:215], v155 offset:7168
	global_load_lds_dwordx4 v140, s[22:23]
	s_add_i32 m0, s21, 0xe000
	s_nop 0
	global_load_lds_dwordx4 v142, s[22:23]
	s_waitcnt vmcnt(8)
	s_waitcnt lgkmcnt(0)
	s_barrier
	s_setprio 1
	s_waitcnt lgkmcnt(0)
	v_mfma_f32_16x16x32_bf16 v[126:129], v[148:151], v[184:187], v[126:129]
	v_mfma_f32_16x16x32_bf16 v[122:125], v[160:163], v[184:187], v[122:125]
	v_mfma_f32_16x16x32_bf16 v[118:121], v[148:151], v[192:195], v[118:121]
	v_mfma_f32_16x16x32_bf16 v[110:113], v[160:163], v[192:195], v[110:113]
	v_mfma_f32_16x16x32_bf16 v[102:105], v[148:151], v[200:203], v[102:105]
	v_mfma_f32_16x16x32_bf16 v[94:97], v[160:163], v[200:203], v[94:97]
	v_mfma_f32_16x16x32_bf16 v[86:89], v[148:151], v[208:211], v[86:89]
	v_mfma_f32_16x16x32_bf16 v[78:81], v[160:163], v[208:211], v[78:81]
	v_mfma_f32_16x16x32_bf16 v[126:129], v[156:159], v[188:191], v[126:129]
	v_mfma_f32_16x16x32_bf16 v[122:125], v[164:167], v[188:191], v[122:125]
	v_mfma_f32_16x16x32_bf16 v[118:121], v[156:159], v[196:199], v[118:121]
	v_mfma_f32_16x16x32_bf16 v[110:113], v[164:167], v[196:199], v[110:113]
	v_mfma_f32_16x16x32_bf16 v[102:105], v[156:159], v[204:207], v[102:105]
	v_mfma_f32_16x16x32_bf16 v[94:97], v[164:167], v[204:207], v[94:97]
	v_mfma_f32_16x16x32_bf16 v[86:89], v[156:159], v[212:215], v[86:89]
	v_mfma_f32_16x16x32_bf16 v[78:81], v[164:167], v[212:215], v[78:81]
	s_setprio 0
	s_setprio 1
	v_mfma_f32_16x16x32_bf16 v[114:117], v[168:171], v[184:187], v[114:117]
	v_mfma_f32_16x16x32_bf16 v[106:109], v[176:179], v[184:187], v[106:109]
	v_mfma_f32_16x16x32_bf16 v[98:101], v[168:171], v[192:195], v[98:101]
	v_mfma_f32_16x16x32_bf16 v[90:93], v[176:179], v[192:195], v[90:93]
	v_mfma_f32_16x16x32_bf16 v[82:85], v[168:171], v[200:203], v[82:85]
	v_mfma_f32_16x16x32_bf16 v[74:77], v[176:179], v[200:203], v[74:77]
	v_mfma_f32_16x16x32_bf16 v[70:73], v[168:171], v[208:211], v[70:73]
	v_mfma_f32_16x16x32_bf16 v[66:69], v[176:179], v[208:211], v[66:69]
	v_mfma_f32_16x16x32_bf16 v[114:117], v[172:175], v[188:191], v[114:117]
	v_mfma_f32_16x16x32_bf16 v[106:109], v[180:183], v[188:191], v[106:109]
	v_mfma_f32_16x16x32_bf16 v[98:101], v[172:175], v[196:199], v[98:101]
	v_mfma_f32_16x16x32_bf16 v[90:93], v[180:183], v[196:199], v[90:93]
	v_mfma_f32_16x16x32_bf16 v[82:85], v[172:175], v[204:207], v[82:85]
	v_mfma_f32_16x16x32_bf16 v[74:77], v[180:183], v[204:207], v[74:77]
	v_mfma_f32_16x16x32_bf16 v[70:73], v[172:175], v[212:215], v[70:73]
	v_mfma_f32_16x16x32_bf16 v[66:69], v[180:183], v[212:215], v[66:69]
	s_setprio 0
	s_barrier
	s_add_i32 s80, s71, s33
	v_lshl_add_u64 v[216:217], s[24:25], 0, v[136:137]
	s_mov_b32 m0, s80
	ds_read_b128 v[184:187], v155 offset:16384
	ds_read_b128 v[188:191], v155 offset:17408
	ds_read_b128 v[192:195], v155 offset:18432
	ds_read_b128 v[196:199], v155 offset:19456
	ds_read_b128 v[200:203], v155 offset:20480
	ds_read_b128 v[204:207], v155 offset:21504
	ds_read_b128 v[208:211], v155 offset:22528
	ds_read_b128 v[212:215], v155 offset:23552
	global_load_lds_dwordx4 v136, s[24:25]
	s_add_i32 m0, s80, 0x2000
	s_add_u32 s80, s24, 0x80000
	v_lshl_add_u64 v[218:219], s[24:25], 0, v[132:133]
	s_addc_u32 s81, s25, 0
	s_add_i32 s82, s72, s33
	global_load_lds_dwordx4 v132, s[24:25]
	s_mov_b32 m0, s82
	v_lshl_add_u64 v[222:223], s[26:27], 0, v[134:135]
	global_load_lds_dwordx4 v136, s[80:81]
	s_add_i32 m0, s82, 0x2000
	s_nop 0
	global_load_lds_dwordx4 v132, s[80:81]
	v_lshl_add_u64 v[220:221], s[26:27], 0, v[138:139]
	s_mov_b32 m0, s21
	s_nop 0
	global_load_lds_dwordx4 v138, s[26:27]
	s_mov_b32 m0, s36
	s_nop 0
	global_load_lds_dwordx4 v134, s[26:27]
	s_waitcnt vmcnt(8)
	s_waitcnt lgkmcnt(0)
	s_barrier
	s_setprio 1
	s_waitcnt lgkmcnt(0)
	v_mfma_f32_16x16x32_bf16 v[62:65], v[148:151], v[184:187], v[62:65]
	v_mfma_f32_16x16x32_bf16 v[58:61], v[160:163], v[184:187], v[58:61]
	v_mfma_f32_16x16x32_bf16 v[54:57], v[148:151], v[192:195], v[54:57]
	v_mfma_f32_16x16x32_bf16 v[46:49], v[160:163], v[192:195], v[46:49]
	v_mfma_f32_16x16x32_bf16 v[38:41], v[148:151], v[200:203], v[38:41]
	v_mfma_f32_16x16x32_bf16 v[30:33], v[160:163], v[200:203], v[30:33]
	v_mfma_f32_16x16x32_bf16 v[22:25], v[148:151], v[208:211], v[22:25]
	v_mfma_f32_16x16x32_bf16 v[14:17], v[160:163], v[208:211], v[14:17]
	v_mfma_f32_16x16x32_bf16 v[62:65], v[156:159], v[188:191], v[62:65]
	v_mfma_f32_16x16x32_bf16 v[58:61], v[164:167], v[188:191], v[58:61]
	v_mfma_f32_16x16x32_bf16 v[54:57], v[156:159], v[196:199], v[54:57]
	v_mfma_f32_16x16x32_bf16 v[46:49], v[164:167], v[196:199], v[46:49]
	v_mfma_f32_16x16x32_bf16 v[38:41], v[156:159], v[204:207], v[38:41]
	v_mfma_f32_16x16x32_bf16 v[30:33], v[164:167], v[204:207], v[30:33]
	v_mfma_f32_16x16x32_bf16 v[22:25], v[156:159], v[212:215], v[22:25]
	v_mfma_f32_16x16x32_bf16 v[14:17], v[164:167], v[212:215], v[14:17]
	s_setprio 0
	s_setprio 1
	v_mfma_f32_16x16x32_bf16 v[50:53], v[168:171], v[184:187], v[50:53]
	v_mfma_f32_16x16x32_bf16 v[42:45], v[176:179], v[184:187], v[42:45]
	v_mfma_f32_16x16x32_bf16 v[34:37], v[168:171], v[192:195], v[34:37]
	v_mfma_f32_16x16x32_bf16 v[26:29], v[176:179], v[192:195], v[26:29]
	v_mfma_f32_16x16x32_bf16 v[18:21], v[168:171], v[200:203], v[18:21]
	v_mfma_f32_16x16x32_bf16 v[10:13], v[176:179], v[200:203], v[10:13]
	v_mfma_f32_16x16x32_bf16 v[6:9], v[168:171], v[208:211], v[6:9]
	v_mfma_f32_16x16x32_bf16 v[2:5], v[176:179], v[208:211], v[2:5]
	v_mfma_f32_16x16x32_bf16 v[50:53], v[172:175], v[188:191], v[50:53]
	v_mfma_f32_16x16x32_bf16 v[42:45], v[180:183], v[188:191], v[42:45]
	v_mfma_f32_16x16x32_bf16 v[34:37], v[172:175], v[196:199], v[34:37]
	v_mfma_f32_16x16x32_bf16 v[26:29], v[180:183], v[196:199], v[26:29]
	v_mfma_f32_16x16x32_bf16 v[18:21], v[172:175], v[204:207], v[18:21]
	v_mfma_f32_16x16x32_bf16 v[10:13], v[180:183], v[204:207], v[10:13]
	v_mfma_f32_16x16x32_bf16 v[6:9], v[172:175], v[212:215], v[6:9]
	v_mfma_f32_16x16x32_bf16 v[2:5], v[180:183], v[212:215], v[2:5]
	s_setprio 0
	s_barrier
	s_add_i32 s80, 0, 0x18000
	s_add_i32 s81, 0, 0x1c000
	v_add_u32_e32 v164, s80, v131
	v_add_u32_e32 v180, s81, v131
	ds_read_b128 v[148:151], v164
	ds_read_b128 v[156:159], v164 offset:1024
	ds_read_b128 v[160:163], v164 offset:2048
	ds_read_b128 v[164:167], v164 offset:3072
	ds_read_b128 v[168:171], v180
	ds_read_b128 v[172:175], v180 offset:1024
	ds_read_b128 v[176:179], v180 offset:2048
	ds_read_b128 v[180:183], v180 offset:3072
	s_add_u32 s26, s26, 0x80000
	s_addc_u32 s27, s27, 0
	s_mov_b32 m0, s37
	ds_read_b128 v[184:187], v155 offset:32768
	ds_read_b128 v[188:191], v155 offset:33792
	ds_read_b128 v[192:195], v155 offset:34816
	ds_read_b128 v[196:199], v155 offset:35840
	ds_read_b128 v[200:203], v155 offset:36864
	ds_read_b128 v[204:207], v155 offset:37888
	ds_read_b128 v[208:211], v155 offset:38912
	ds_read_b128 v[212:215], v155 offset:39936
	global_load_lds_dwordx4 v138, s[26:27]
	s_mov_b32 m0, s42
	s_nop 0
	global_load_lds_dwordx4 v134, s[26:27]
	s_waitcnt vmcnt(8)
	s_waitcnt lgkmcnt(0)
	s_barrier
	s_setprio 1
	s_waitcnt lgkmcnt(0)
	v_mfma_f32_16x16x32_bf16 v[126:129], v[148:151], v[184:187], v[126:129]
	v_mfma_f32_16x16x32_bf16 v[122:125], v[160:163], v[184:187], v[122:125]
	v_mfma_f32_16x16x32_bf16 v[118:121], v[148:151], v[192:195], v[118:121]
	v_mfma_f32_16x16x32_bf16 v[110:113], v[160:163], v[192:195], v[110:113]
	v_mfma_f32_16x16x32_bf16 v[102:105], v[148:151], v[200:203], v[102:105]
	v_mfma_f32_16x16x32_bf16 v[94:97], v[160:163], v[200:203], v[94:97]
	v_mfma_f32_16x16x32_bf16 v[86:89], v[148:151], v[208:211], v[86:89]
	v_mfma_f32_16x16x32_bf16 v[78:81], v[160:163], v[208:211], v[78:81]
	v_mfma_f32_16x16x32_bf16 v[126:129], v[156:159], v[188:191], v[126:129]
	v_mfma_f32_16x16x32_bf16 v[122:125], v[164:167], v[188:191], v[122:125]
	v_mfma_f32_16x16x32_bf16 v[118:121], v[156:159], v[196:199], v[118:121]
	v_mfma_f32_16x16x32_bf16 v[110:113], v[164:167], v[196:199], v[110:113]
	v_mfma_f32_16x16x32_bf16 v[102:105], v[156:159], v[204:207], v[102:105]
	v_mfma_f32_16x16x32_bf16 v[94:97], v[164:167], v[204:207], v[94:97]
	v_mfma_f32_16x16x32_bf16 v[86:89], v[156:159], v[212:215], v[86:89]
	v_mfma_f32_16x16x32_bf16 v[78:81], v[164:167], v[212:215], v[78:81]
	s_setprio 0
	s_setprio 1
	v_mfma_f32_16x16x32_bf16 v[114:117], v[168:171], v[184:187], v[114:117]
	v_mfma_f32_16x16x32_bf16 v[106:109], v[176:179], v[184:187], v[106:109]
	v_mfma_f32_16x16x32_bf16 v[98:101], v[168:171], v[192:195], v[98:101]
	v_mfma_f32_16x16x32_bf16 v[90:93], v[176:179], v[192:195], v[90:93]
	v_mfma_f32_16x16x32_bf16 v[82:85], v[168:171], v[200:203], v[82:85]
	v_mfma_f32_16x16x32_bf16 v[74:77], v[176:179], v[200:203], v[74:77]
	v_mfma_f32_16x16x32_bf16 v[70:73], v[168:171], v[208:211], v[70:73]
	v_mfma_f32_16x16x32_bf16 v[66:69], v[176:179], v[208:211], v[66:69]
	v_mfma_f32_16x16x32_bf16 v[114:117], v[172:175], v[188:191], v[114:117]
	v_mfma_f32_16x16x32_bf16 v[106:109], v[180:183], v[188:191], v[106:109]
	v_mfma_f32_16x16x32_bf16 v[98:101], v[172:175], v[196:199], v[98:101]
	v_mfma_f32_16x16x32_bf16 v[90:93], v[180:183], v[196:199], v[90:93]
	v_mfma_f32_16x16x32_bf16 v[82:85], v[172:175], v[204:207], v[82:85]
	v_mfma_f32_16x16x32_bf16 v[74:77], v[180:183], v[204:207], v[74:77]
	v_mfma_f32_16x16x32_bf16 v[70:73], v[172:175], v[212:215], v[70:73]
	v_mfma_f32_16x16x32_bf16 v[66:69], v[180:183], v[212:215], v[66:69]
	s_setprio 0
	s_barrier
	s_add_i32 s26, s80, s33
	v_lshl_add_u64 v[216:217], v[216:217], 0, s[8:9]
	s_mov_b32 m0, s26
	ds_read_b128 v[184:187], v155 offset:49152
	ds_read_b128 v[188:191], v155 offset:50176
	ds_read_b128 v[192:195], v155 offset:51200
	ds_read_b128 v[196:199], v155 offset:52224
	ds_read_b128 v[200:203], v155 offset:53248
	ds_read_b128 v[204:207], v155 offset:54272
	ds_read_b128 v[208:211], v155 offset:55296
	ds_read_b128 v[212:215], v155 offset:56320
	global_load_lds_dwordx4 v[216:217], off
	s_add_i32 m0, s26, 0x2000
	s_add_u32 s24, s24, 0x80080
	v_lshl_add_u64 v[216:217], v[218:219], 0, s[8:9]
	s_addc_u32 s25, s25, 0
	s_add_i32 s26, s81, s33
	global_load_lds_dwordx4 v[216:217], off
	s_mov_b32 m0, s26
	s_nop 0
	global_load_lds_dwordx4 v136, s[24:25]
	s_add_i32 m0, s26, 0x2000
	s_nop 0
	global_load_lds_dwordx4 v132, s[24:25]
	v_lshl_add_u64 v[216:217], v[220:221], 0, s[8:9]
	s_mov_b32 m0, s44
	s_nop 0
	global_load_lds_dwordx4 v[216:217], off
	v_lshl_add_u64 v[216:217], v[222:223], 0, s[8:9]
	s_mov_b32 m0, s45
	s_nop 0
	global_load_lds_dwordx4 v[216:217], off
	s_waitcnt vmcnt(8)
	s_waitcnt lgkmcnt(0)
	s_barrier
	s_setprio 1
	s_waitcnt lgkmcnt(0)
	v_mfma_f32_16x16x32_bf16 v[62:65], v[148:151], v[184:187], v[62:65]
	v_mfma_f32_16x16x32_bf16 v[58:61], v[160:163], v[184:187], v[58:61]
	v_mfma_f32_16x16x32_bf16 v[54:57], v[148:151], v[192:195], v[54:57]
	v_mfma_f32_16x16x32_bf16 v[46:49], v[160:163], v[192:195], v[46:49]
	v_mfma_f32_16x16x32_bf16 v[38:41], v[148:151], v[200:203], v[38:41]
	v_mfma_f32_16x16x32_bf16 v[30:33], v[160:163], v[200:203], v[30:33]
	v_mfma_f32_16x16x32_bf16 v[22:25], v[148:151], v[208:211], v[22:25]
	v_mfma_f32_16x16x32_bf16 v[14:17], v[160:163], v[208:211], v[14:17]
	v_mfma_f32_16x16x32_bf16 v[62:65], v[156:159], v[188:191], v[62:65]
	v_mfma_f32_16x16x32_bf16 v[58:61], v[164:167], v[188:191], v[58:61]
	v_mfma_f32_16x16x32_bf16 v[54:57], v[156:159], v[196:199], v[54:57]
	v_mfma_f32_16x16x32_bf16 v[46:49], v[164:167], v[196:199], v[46:49]
	v_mfma_f32_16x16x32_bf16 v[38:41], v[156:159], v[204:207], v[38:41]
	v_mfma_f32_16x16x32_bf16 v[30:33], v[164:167], v[204:207], v[30:33]
	v_mfma_f32_16x16x32_bf16 v[22:25], v[156:159], v[212:215], v[22:25]
	v_mfma_f32_16x16x32_bf16 v[14:17], v[164:167], v[212:215], v[14:17]
	s_setprio 0
	s_setprio 1
	v_mfma_f32_16x16x32_bf16 v[50:53], v[168:171], v[184:187], v[50:53]
	v_mfma_f32_16x16x32_bf16 v[42:45], v[176:179], v[184:187], v[42:45]
	v_mfma_f32_16x16x32_bf16 v[34:37], v[168:171], v[192:195], v[34:37]
	v_mfma_f32_16x16x32_bf16 v[26:29], v[176:179], v[192:195], v[26:29]
	v_mfma_f32_16x16x32_bf16 v[18:21], v[168:171], v[200:203], v[18:21]
	v_mfma_f32_16x16x32_bf16 v[10:13], v[176:179], v[200:203], v[10:13]
	v_mfma_f32_16x16x32_bf16 v[6:9], v[168:171], v[208:211], v[6:9]
	v_mfma_f32_16x16x32_bf16 v[2:5], v[176:179], v[208:211], v[2:5]
	v_mfma_f32_16x16x32_bf16 v[50:53], v[172:175], v[188:191], v[50:53]
	v_mfma_f32_16x16x32_bf16 v[42:45], v[180:183], v[188:191], v[42:45]
	v_mfma_f32_16x16x32_bf16 v[34:37], v[172:175], v[196:199], v[34:37]
	v_mfma_f32_16x16x32_bf16 v[26:29], v[180:183], v[196:199], v[26:29]
	v_mfma_f32_16x16x32_bf16 v[18:21], v[172:175], v[204:207], v[18:21]
	v_mfma_f32_16x16x32_bf16 v[10:13], v[180:183], v[204:207], v[10:13]
	v_mfma_f32_16x16x32_bf16 v[6:9], v[172:175], v[212:215], v[6:9]
	v_mfma_f32_16x16x32_bf16 v[2:5], v[180:183], v[212:215], v[2:5]
	s_setprio 0
	s_barrier
	s_add_i32 s79, s79, 2
	s_add_u32 s22, s22, 0x100
	s_addc_u32 s23, s23, 0
	s_add_u32 s77, s77, 0x100
	s_addc_u32 s78, s78, 0
	s_cmp_gt_u32 s79, 29
	s_cbranch_scc0 .LBB0_119
	s_and_b64 vcc, exec, s[10:11]
	s_cbranch_vccz .LBB0_122
	s_barrier

.LBB0_466:
	ds_read_b128 v[150:153], v211
	ds_read_b128 v[154:157], v211 offset:1024
	ds_read_b128 v[158:161], v211 offset:2048
	ds_read_b128 v[162:165], v211 offset:3072
	ds_read_b128 v[166:169], v212
	ds_read_b128 v[170:173], v212 offset:1024
	ds_read_b128 v[174:177], v212 offset:2048
	ds_read_b128 v[178:181], v212 offset:3072
	s_add_u32 s42, s36, 0xfff80080
	s_addc_u32 s43, s37, -1
	s_cmp_eq_u32 s83, 28
	s_cselect_b32 s45, s1, s43
	s_cselect_b32 s44, s27, s42
	s_cselect_b32 s43, s25, s63
	s_cselect_b32 s42, s35, s62
	s_add_i32 m0, s67, 0xc000
	ds_read_b128 v[182:185], v213
	ds_read_b128 v[186:189], v213 offset:1024
	ds_read_b128 v[190:193], v213 offset:2048
	ds_read_b128 v[194:197], v213 offset:3072
	ds_read_b128 v[198:201], v213 offset:4096
	ds_read_b128 v[202:205], v213 offset:5120
	ds_read_b128 v[218:221], v213 offset:6144
	ds_read_b128 v[222:225], v213 offset:7168
	global_load_lds_dwordx4 v142, s[36:37]
	s_add_i32 m0, s67, 0xe000
	s_nop 0
	global_load_lds_dwordx4 v144, s[36:37]
	s_waitcnt vmcnt(8)
	s_waitcnt lgkmcnt(0)
	s_barrier
	s_setprio 1
	s_waitcnt lgkmcnt(0)
	v_mfma_f32_16x16x32_bf16 v[126:129], v[150:153], v[182:185], v[126:129]
	v_mfma_f32_16x16x32_bf16 v[122:125], v[158:161], v[182:185], v[122:125]
	v_mfma_f32_16x16x32_bf16 v[110:113], v[150:153], v[190:193], v[110:113]
	v_mfma_f32_16x16x32_bf16 v[106:109], v[158:161], v[190:193], v[106:109]
	v_mfma_f32_16x16x32_bf16 v[94:97], v[150:153], v[198:201], v[94:97]
	v_mfma_f32_16x16x32_bf16 v[90:93], v[158:161], v[198:201], v[90:93]
	v_mfma_f32_16x16x32_bf16 v[78:81], v[150:153], v[218:221], v[78:81]
	v_mfma_f32_16x16x32_bf16 v[74:77], v[158:161], v[218:221], v[74:77]
	v_mfma_f32_16x16x32_bf16 v[126:129], v[154:157], v[186:189], v[126:129]
	v_mfma_f32_16x16x32_bf16 v[122:125], v[162:165], v[186:189], v[122:125]
	v_mfma_f32_16x16x32_bf16 v[110:113], v[154:157], v[194:197], v[110:113]
	v_mfma_f32_16x16x32_bf16 v[106:109], v[162:165], v[194:197], v[106:109]
	v_mfma_f32_16x16x32_bf16 v[94:97], v[154:157], v[202:205], v[94:97]
	v_mfma_f32_16x16x32_bf16 v[90:93], v[162:165], v[202:205], v[90:93]
	v_mfma_f32_16x16x32_bf16 v[78:81], v[154:157], v[222:225], v[78:81]
	v_mfma_f32_16x16x32_bf16 v[74:77], v[162:165], v[222:225], v[74:77]
	s_setprio 0
	s_setprio 1
	v_mfma_f32_16x16x32_bf16 v[118:121], v[166:169], v[182:185], v[118:121]
	v_mfma_f32_16x16x32_bf16 v[114:117], v[174:177], v[182:185], v[114:117]
	v_mfma_f32_16x16x32_bf16 v[102:105], v[166:169], v[190:193], v[102:105]
	v_mfma_f32_16x16x32_bf16 v[98:101], v[174:177], v[190:193], v[98:101]
	v_mfma_f32_16x16x32_bf16 v[86:89], v[166:169], v[198:201], v[86:89]
	v_mfma_f32_16x16x32_bf16 v[82:85], v[174:177], v[198:201], v[82:85]
	v_mfma_f32_16x16x32_bf16 v[70:73], v[166:169], v[218:221], v[70:73]
	v_mfma_f32_16x16x32_bf16 v[66:69], v[174:177], v[218:221], v[66:69]
	v_mfma_f32_16x16x32_bf16 v[118:121], v[170:173], v[186:189], v[118:121]
	v_mfma_f32_16x16x32_bf16 v[114:117], v[178:181], v[186:189], v[114:117]
	v_mfma_f32_16x16x32_bf16 v[102:105], v[170:173], v[194:197], v[102:105]
	v_mfma_f32_16x16x32_bf16 v[98:101], v[178:181], v[194:197], v[98:101]
	v_mfma_f32_16x16x32_bf16 v[86:89], v[170:173], v[202:205], v[86:89]
	v_mfma_f32_16x16x32_bf16 v[82:85], v[178:181], v[202:205], v[82:85]
	v_mfma_f32_16x16x32_bf16 v[70:73], v[170:173], v[222:225], v[70:73]
	v_mfma_f32_16x16x32_bf16 v[66:69], v[178:181], v[222:225], v[66:69]
	s_setprio 0
	s_barrier
	s_add_i32 s84, s79, s66
	v_lshl_add_u64 v[226:227], s[42:43], 0, v[132:133]
	s_mov_b32 m0, s84
	ds_read_b128 v[182:185], v213 offset:16384
	ds_read_b128 v[186:189], v213 offset:17408
	ds_read_b128 v[190:193], v213 offset:18432
	ds_read_b128 v[194:197], v213 offset:19456
	ds_read_b128 v[198:201], v213 offset:20480
	ds_read_b128 v[202:205], v213 offset:21504
	ds_read_b128 v[218:221], v213 offset:22528
	ds_read_b128 v[222:225], v213 offset:23552
	global_load_lds_dwordx4 v132, s[42:43]
	s_add_i32 m0, s84, 0x2000
	s_add_u32 s84, s42, 0x80000
	v_lshl_add_u64 v[228:229], s[42:43], 0, v[136:137]
	s_addc_u32 s85, s43, 0
	s_add_i32 s86, s80, s66
	global_load_lds_dwordx4 v136, s[42:43]
	s_mov_b32 m0, s86
	v_lshl_add_u64 v[232:233], s[44:45], 0, v[134:135]
	global_load_lds_dwordx4 v132, s[84:85]
	s_add_i32 m0, s86, 0x2000
	s_nop 0
	global_load_lds_dwordx4 v136, s[84:85]
	v_lshl_add_u64 v[230:231], s[44:45], 0, v[130:131]
	s_mov_b32 m0, s67
	s_nop 0
	global_load_lds_dwordx4 v130, s[44:45]
	s_mov_b32 m0, s68
	s_nop 0
	global_load_lds_dwordx4 v134, s[44:45]
	s_waitcnt vmcnt(8)
	s_waitcnt lgkmcnt(0)
	s_barrier
	s_setprio 1
	s_waitcnt lgkmcnt(0)
	v_mfma_f32_16x16x32_bf16 v[62:65], v[150:153], v[182:185], v[62:65]
	v_mfma_f32_16x16x32_bf16 v[58:61], v[158:161], v[182:185], v[58:61]
	v_mfma_f32_16x16x32_bf16 v[46:49], v[150:153], v[190:193], v[46:49]
	v_mfma_f32_16x16x32_bf16 v[42:45], v[158:161], v[190:193], v[42:45]
	v_mfma_f32_16x16x32_bf16 v[30:33], v[150:153], v[198:201], v[30:33]
	v_mfma_f32_16x16x32_bf16 v[26:29], v[158:161], v[198:201], v[26:29]
	v_mfma_f32_16x16x32_bf16 v[14:17], v[150:153], v[218:221], v[14:17]
	v_mfma_f32_16x16x32_bf16 v[10:13], v[158:161], v[218:221], v[10:13]
	v_mfma_f32_16x16x32_bf16 v[62:65], v[154:157], v[186:189], v[62:65]
	v_mfma_f32_16x16x32_bf16 v[58:61], v[162:165], v[186:189], v[58:61]
	v_mfma_f32_16x16x32_bf16 v[46:49], v[154:157], v[194:197], v[46:49]
	v_mfma_f32_16x16x32_bf16 v[42:45], v[162:165], v[194:197], v[42:45]
	v_mfma_f32_16x16x32_bf16 v[30:33], v[154:157], v[202:205], v[30:33]
	v_mfma_f32_16x16x32_bf16 v[26:29], v[162:165], v[202:205], v[26:29]
	v_mfma_f32_16x16x32_bf16 v[14:17], v[154:157], v[222:225], v[14:17]
	v_mfma_f32_16x16x32_bf16 v[10:13], v[162:165], v[222:225], v[10:13]
	s_setprio 0
	s_setprio 1
	v_mfma_f32_16x16x32_bf16 v[54:57], v[166:169], v[182:185], v[54:57]
	v_mfma_f32_16x16x32_bf16 v[50:53], v[174:177], v[182:185], v[50:53]
	v_mfma_f32_16x16x32_bf16 v[38:41], v[166:169], v[190:193], v[38:41]
	v_mfma_f32_16x16x32_bf16 v[34:37], v[174:177], v[190:193], v[34:37]
	v_mfma_f32_16x16x32_bf16 v[22:25], v[166:169], v[198:201], v[22:25]
	v_mfma_f32_16x16x32_bf16 v[18:21], v[174:177], v[198:201], v[18:21]
	v_mfma_f32_16x16x32_bf16 v[6:9], v[166:169], v[218:221], v[6:9]
	v_mfma_f32_16x16x32_bf16 v[2:5], v[174:177], v[218:221], v[2:5]
	v_mfma_f32_16x16x32_bf16 v[54:57], v[170:173], v[186:189], v[54:57]
	v_mfma_f32_16x16x32_bf16 v[50:53], v[178:181], v[186:189], v[50:53]
	v_mfma_f32_16x16x32_bf16 v[38:41], v[170:173], v[194:197], v[38:41]
	v_mfma_f32_16x16x32_bf16 v[34:37], v[178:181], v[194:197], v[34:37]
	v_mfma_f32_16x16x32_bf16 v[22:25], v[170:173], v[202:205], v[22:25]
	v_mfma_f32_16x16x32_bf16 v[18:21], v[178:181], v[202:205], v[18:21]
	v_mfma_f32_16x16x32_bf16 v[6:9], v[170:173], v[222:225], v[6:9]
	v_mfma_f32_16x16x32_bf16 v[2:5], v[178:181], v[222:225], v[2:5]
	s_setprio 0
	s_barrier
	s_add_i32 s84, 0, 0x18000
	v_add_u32_e32 v139, s84, v206
	s_add_i32 s85, 0, 0x1c000
	ds_read_b128 v[150:153], v139
	ds_read_b128 v[154:157], v139 offset:1024
	ds_read_b128 v[158:161], v139 offset:2048
	ds_read_b128 v[162:165], v139 offset:3072
	v_add_u32_e32 v139, s85, v206
	ds_read_b128 v[166:169], v139
	ds_read_b128 v[170:173], v139 offset:1024
	ds_read_b128 v[174:177], v139 offset:2048
	ds_read_b128 v[178:181], v139 offset:3072
	s_add_u32 s44, s44, 0x80000
	s_addc_u32 s45, s45, 0
	s_mov_b32 m0, s69
	ds_read_b128 v[182:185], v213 offset:32768
	ds_read_b128 v[186:189], v213 offset:33792
	ds_read_b128 v[190:193], v213 offset:34816
	ds_read_b128 v[194:197], v213 offset:35840
	ds_read_b128 v[198:201], v213 offset:36864
	ds_read_b128 v[202:205], v213 offset:37888
	ds_read_b128 v[218:221], v213 offset:38912
	ds_read_b128 v[222:225], v213 offset:39936
	global_load_lds_dwordx4 v130, s[44:45]
	s_mov_b32 m0, s70
	s_nop 0
	global_load_lds_dwordx4 v134, s[44:45]
	s_waitcnt vmcnt(8)
	s_waitcnt lgkmcnt(0)
	s_barrier
	s_setprio 1
	s_waitcnt lgkmcnt(0)
	v_mfma_f32_16x16x32_bf16 v[126:129], v[150:153], v[182:185], v[126:129]
	v_mfma_f32_16x16x32_bf16 v[122:125], v[158:161], v[182:185], v[122:125]
	v_mfma_f32_16x16x32_bf16 v[110:113], v[150:153], v[190:193], v[110:113]
	v_mfma_f32_16x16x32_bf16 v[106:109], v[158:161], v[190:193], v[106:109]
	v_mfma_f32_16x16x32_bf16 v[94:97], v[150:153], v[198:201], v[94:97]
	v_mfma_f32_16x16x32_bf16 v[90:93], v[158:161], v[198:201], v[90:93]
	v_mfma_f32_16x16x32_bf16 v[78:81], v[150:153], v[218:221], v[78:81]
	v_mfma_f32_16x16x32_bf16 v[74:77], v[158:161], v[218:221], v[74:77]
	v_mfma_f32_16x16x32_bf16 v[126:129], v[154:157], v[186:189], v[126:129]
	v_mfma_f32_16x16x32_bf16 v[122:125], v[162:165], v[186:189], v[122:125]
	v_mfma_f32_16x16x32_bf16 v[110:113], v[154:157], v[194:197], v[110:113]
	v_mfma_f32_16x16x32_bf16 v[106:109], v[162:165], v[194:197], v[106:109]
	v_mfma_f32_16x16x32_bf16 v[94:97], v[154:157], v[202:205], v[94:97]
	v_mfma_f32_16x16x32_bf16 v[90:93], v[162:165], v[202:205], v[90:93]
	v_mfma_f32_16x16x32_bf16 v[78:81], v[154:157], v[222:225], v[78:81]
	v_mfma_f32_16x16x32_bf16 v[74:77], v[162:165], v[222:225], v[74:77]
	s_setprio 0
	s_setprio 1
	v_mfma_f32_16x16x32_bf16 v[118:121], v[166:169], v[182:185], v[118:121]
	v_mfma_f32_16x16x32_bf16 v[114:117], v[174:177], v[182:185], v[114:117]
	v_mfma_f32_16x16x32_bf16 v[102:105], v[166:169], v[190:193], v[102:105]
	v_mfma_f32_16x16x32_bf16 v[98:101], v[174:177], v[190:193], v[98:101]
	v_mfma_f32_16x16x32_bf16 v[86:89], v[166:169], v[198:201], v[86:89]
	v_mfma_f32_16x16x32_bf16 v[82:85], v[174:177], v[198:201], v[82:85]
	v_mfma_f32_16x16x32_bf16 v[70:73], v[166:169], v[218:221], v[70:73]
	v_mfma_f32_16x16x32_bf16 v[66:69], v[174:177], v[218:221], v[66:69]
	v_mfma_f32_16x16x32_bf16 v[118:121], v[170:173], v[186:189], v[118:121]
	v_mfma_f32_16x16x32_bf16 v[114:117], v[178:181], v[186:189], v[114:117]
	v_mfma_f32_16x16x32_bf16 v[102:105], v[170:173], v[194:197], v[102:105]
	v_mfma_f32_16x16x32_bf16 v[98:101], v[178:181], v[194:197], v[98:101]
	v_mfma_f32_16x16x32_bf16 v[86:89], v[170:173], v[202:205], v[86:89]
	v_mfma_f32_16x16x32_bf16 v[82:85], v[178:181], v[202:205], v[82:85]
	v_mfma_f32_16x16x32_bf16 v[70:73], v[170:173], v[222:225], v[70:73]
	v_mfma_f32_16x16x32_bf16 v[66:69], v[178:181], v[222:225], v[66:69]
	s_setprio 0
	s_barrier
	s_add_i32 s44, s84, s66
	v_lshl_add_u64 v[226:227], v[226:227], 0, s[18:19]
	s_mov_b32 m0, s44
	ds_read_b128 v[182:185], v213 offset:49152
	ds_read_b128 v[186:189], v213 offset:50176
	ds_read_b128 v[190:193], v213 offset:51200
	ds_read_b128 v[194:197], v213 offset:52224
	ds_read_b128 v[198:201], v213 offset:53248
	ds_read_b128 v[202:205], v213 offset:54272
	ds_read_b128 v[218:221], v213 offset:55296
	ds_read_b128 v[222:225], v213 offset:56320
	global_load_lds_dwordx4 v[226:227], off
	s_add_i32 m0, s44, 0x2000
	s_add_u32 s42, s42, 0x80080
	v_lshl_add_u64 v[226:227], v[228:229], 0, s[18:19]
	s_addc_u32 s43, s43, 0
	s_add_i32 s44, s85, s66
	global_load_lds_dwordx4 v[226:227], off
	s_mov_b32 m0, s44
	s_nop 0
	global_load_lds_dwordx4 v132, s[42:43]
	s_add_i32 m0, s44, 0x2000
	s_nop 0
	global_load_lds_dwordx4 v136, s[42:43]
	v_lshl_add_u64 v[226:227], v[230:231], 0, s[18:19]
	s_mov_b32 m0, s74
	s_nop 0
	global_load_lds_dwordx4 v[226:227], off
	v_lshl_add_u64 v[226:227], v[232:233], 0, s[18:19]
	s_mov_b32 m0, s75
	s_nop 0
	global_load_lds_dwordx4 v[226:227], off
	s_waitcnt vmcnt(8)
	s_waitcnt lgkmcnt(0)
	s_barrier
	s_setprio 1
	s_waitcnt lgkmcnt(0)
	v_mfma_f32_16x16x32_bf16 v[62:65], v[150:153], v[182:185], v[62:65]
	v_mfma_f32_16x16x32_bf16 v[58:61], v[158:161], v[182:185], v[58:61]
	v_mfma_f32_16x16x32_bf16 v[46:49], v[150:153], v[190:193], v[46:49]
	v_mfma_f32_16x16x32_bf16 v[42:45], v[158:161], v[190:193], v[42:45]
	v_mfma_f32_16x16x32_bf16 v[30:33], v[150:153], v[198:201], v[30:33]
	v_mfma_f32_16x16x32_bf16 v[26:29], v[158:161], v[198:201], v[26:29]
	v_mfma_f32_16x16x32_bf16 v[14:17], v[150:153], v[218:221], v[14:17]
	v_mfma_f32_16x16x32_bf16 v[10:13], v[158:161], v[218:221], v[10:13]
	v_mfma_f32_16x16x32_bf16 v[62:65], v[154:157], v[186:189], v[62:65]
	v_mfma_f32_16x16x32_bf16 v[58:61], v[162:165], v[186:189], v[58:61]
	v_mfma_f32_16x16x32_bf16 v[46:49], v[154:157], v[194:197], v[46:49]
	v_mfma_f32_16x16x32_bf16 v[42:45], v[162:165], v[194:197], v[42:45]
	v_mfma_f32_16x16x32_bf16 v[30:33], v[154:157], v[202:205], v[30:33]
	v_mfma_f32_16x16x32_bf16 v[26:29], v[162:165], v[202:205], v[26:29]
	v_mfma_f32_16x16x32_bf16 v[14:17], v[154:157], v[222:225], v[14:17]
	v_mfma_f32_16x16x32_bf16 v[10:13], v[162:165], v[222:225], v[10:13]
	s_setprio 0
	s_setprio 1
	v_mfma_f32_16x16x32_bf16 v[54:57], v[166:169], v[182:185], v[54:57]
	v_mfma_f32_16x16x32_bf16 v[50:53], v[174:177], v[182:185], v[50:53]
	v_mfma_f32_16x16x32_bf16 v[38:41], v[166:169], v[190:193], v[38:41]
	v_mfma_f32_16x16x32_bf16 v[34:37], v[174:177], v[190:193], v[34:37]
	v_mfma_f32_16x16x32_bf16 v[22:25], v[166:169], v[198:201], v[22:25]
	v_mfma_f32_16x16x32_bf16 v[18:21], v[174:177], v[198:201], v[18:21]
	v_mfma_f32_16x16x32_bf16 v[6:9], v[166:169], v[218:221], v[6:9]
	v_mfma_f32_16x16x32_bf16 v[2:5], v[174:177], v[218:221], v[2:5]
	v_mfma_f32_16x16x32_bf16 v[54:57], v[170:173], v[186:189], v[54:57]
	v_mfma_f32_16x16x32_bf16 v[50:53], v[178:181], v[186:189], v[50:53]
	v_mfma_f32_16x16x32_bf16 v[38:41], v[170:173], v[194:197], v[38:41]
	v_mfma_f32_16x16x32_bf16 v[34:37], v[178:181], v[194:197], v[34:37]
	v_mfma_f32_16x16x32_bf16 v[22:25], v[170:173], v[202:205], v[22:25]
	v_mfma_f32_16x16x32_bf16 v[18:21], v[178:181], v[202:205], v[18:21]
	v_mfma_f32_16x16x32_bf16 v[6:9], v[170:173], v[222:225], v[6:9]
	v_mfma_f32_16x16x32_bf16 v[2:5], v[178:181], v[222:225], v[2:5]
	s_setprio 0
	s_barrier
	s_add_i32 s83, s83, 2
	s_add_u32 s36, s36, 0x100
	s_addc_u32 s37, s37, 0
	s_add_u32 s62, s62, 0x100
	s_addc_u32 s63, s63, 0
	s_cmp_gt_u32 s83, 29
	s_cbranch_scc0 .LBB0_466
	s_and_b64 vcc, exec, s[20:21]
	s_cbranch_vccz .LBB0_469
	s_barrier

.LBB0_574:
	ds_read_b128 v[146:149], v152
	ds_read_b128 v[156:159], v152 offset:1024
	ds_read_b128 v[160:163], v152 offset:2048
	ds_read_b128 v[164:167], v152 offset:3072
	ds_read_b128 v[168:171], v153
	ds_read_b128 v[172:175], v153 offset:1024
	ds_read_b128 v[176:179], v153 offset:2048
	ds_read_b128 v[180:183], v153 offset:3072
	s_add_u32 s24, s22, 0xfff80080
	s_addc_u32 s25, s23, -1
	s_cmp_eq_u32 s69, 28
	s_cselect_b32 s27, s15, s25
	s_cselect_b32 s26, s65, s24
	s_cselect_b32 s25, s13, s68
	s_cselect_b32 s24, s66, s67
	s_add_i32 m0, s21, 0xc000
	ds_read_b128 v[184:187], v154
	ds_read_b128 v[188:191], v154 offset:1024
	ds_read_b128 v[192:195], v154 offset:2048
	ds_read_b128 v[196:199], v154 offset:3072
	ds_read_b128 v[200:203], v154 offset:4096
	ds_read_b128 v[204:207], v154 offset:5120
	ds_read_b128 v[208:211], v154 offset:6144
	ds_read_b128 v[212:215], v154 offset:7168
	global_load_lds_dwordx4 v138, s[22:23]
	s_add_i32 m0, s21, 0xe000
	s_nop 0
	global_load_lds_dwordx4 v140, s[22:23]
	s_waitcnt vmcnt(8)
	s_waitcnt lgkmcnt(0)
	s_barrier
	s_setprio 1
	s_waitcnt lgkmcnt(0)
	v_mfma_f32_16x16x32_bf16 v[126:129], v[146:149], v[184:187], v[126:129]
	v_mfma_f32_16x16x32_bf16 v[122:125], v[160:163], v[184:187], v[122:125]
	v_mfma_f32_16x16x32_bf16 v[110:113], v[146:149], v[192:195], v[110:113]
	v_mfma_f32_16x16x32_bf16 v[106:109], v[160:163], v[192:195], v[106:109]
	v_mfma_f32_16x16x32_bf16 v[94:97], v[146:149], v[200:203], v[94:97]
	v_mfma_f32_16x16x32_bf16 v[90:93], v[160:163], v[200:203], v[90:93]
	v_mfma_f32_16x16x32_bf16 v[78:81], v[146:149], v[208:211], v[78:81]
	v_mfma_f32_16x16x32_bf16 v[74:77], v[160:163], v[208:211], v[74:77]
	v_mfma_f32_16x16x32_bf16 v[126:129], v[156:159], v[188:191], v[126:129]
	v_mfma_f32_16x16x32_bf16 v[122:125], v[164:167], v[188:191], v[122:125]
	v_mfma_f32_16x16x32_bf16 v[110:113], v[156:159], v[196:199], v[110:113]
	v_mfma_f32_16x16x32_bf16 v[106:109], v[164:167], v[196:199], v[106:109]
	v_mfma_f32_16x16x32_bf16 v[94:97], v[156:159], v[204:207], v[94:97]
	v_mfma_f32_16x16x32_bf16 v[90:93], v[164:167], v[204:207], v[90:93]
	v_mfma_f32_16x16x32_bf16 v[78:81], v[156:159], v[212:215], v[78:81]
	v_mfma_f32_16x16x32_bf16 v[74:77], v[164:167], v[212:215], v[74:77]
	s_setprio 0
	s_setprio 1
	v_mfma_f32_16x16x32_bf16 v[118:121], v[168:171], v[184:187], v[118:121]
	v_mfma_f32_16x16x32_bf16 v[114:117], v[176:179], v[184:187], v[114:117]
	v_mfma_f32_16x16x32_bf16 v[102:105], v[168:171], v[192:195], v[102:105]
	v_mfma_f32_16x16x32_bf16 v[98:101], v[176:179], v[192:195], v[98:101]
	v_mfma_f32_16x16x32_bf16 v[86:89], v[168:171], v[200:203], v[86:89]
	v_mfma_f32_16x16x32_bf16 v[82:85], v[176:179], v[200:203], v[82:85]
	v_mfma_f32_16x16x32_bf16 v[70:73], v[168:171], v[208:211], v[70:73]
	v_mfma_f32_16x16x32_bf16 v[66:69], v[176:179], v[208:211], v[66:69]
	v_mfma_f32_16x16x32_bf16 v[118:121], v[172:175], v[188:191], v[118:121]
	v_mfma_f32_16x16x32_bf16 v[114:117], v[180:183], v[188:191], v[114:117]
	v_mfma_f32_16x16x32_bf16 v[102:105], v[172:175], v[196:199], v[102:105]
	v_mfma_f32_16x16x32_bf16 v[98:101], v[180:183], v[196:199], v[98:101]
	v_mfma_f32_16x16x32_bf16 v[86:89], v[172:175], v[204:207], v[86:89]
	v_mfma_f32_16x16x32_bf16 v[82:85], v[180:183], v[204:207], v[82:85]
	v_mfma_f32_16x16x32_bf16 v[70:73], v[172:175], v[212:215], v[70:73]
	v_mfma_f32_16x16x32_bf16 v[66:69], v[180:183], v[212:215], v[66:69]
	s_setprio 0
	s_barrier
	s_add_i32 s70, s61, s33
	v_lshl_add_u64 v[216:217], s[24:25], 0, v[134:135]
	s_mov_b32 m0, s70
	ds_read_b128 v[184:187], v154 offset:16384
	ds_read_b128 v[188:191], v154 offset:17408
	ds_read_b128 v[192:195], v154 offset:18432
	ds_read_b128 v[196:199], v154 offset:19456
	ds_read_b128 v[200:203], v154 offset:20480
	ds_read_b128 v[204:207], v154 offset:21504
	ds_read_b128 v[208:211], v154 offset:22528
	ds_read_b128 v[212:215], v154 offset:23552
	global_load_lds_dwordx4 v134, s[24:25]
	s_add_i32 m0, s70, 0x2000
	s_add_u32 s70, s24, 0x80000
	v_lshl_add_u64 v[218:219], s[24:25], 0, v[130:131]
	s_addc_u32 s71, s25, 0
	s_add_i32 s72, s62, s33
	global_load_lds_dwordx4 v130, s[24:25]
	s_mov_b32 m0, s72
	v_lshl_add_u64 v[222:223], s[26:27], 0, v[132:133]
	global_load_lds_dwordx4 v134, s[70:71]
	s_add_i32 m0, s72, 0x2000
	s_nop 0
	global_load_lds_dwordx4 v130, s[70:71]
	v_lshl_add_u64 v[220:221], s[26:27], 0, v[136:137]
	s_mov_b32 m0, s21
	s_nop 0
	global_load_lds_dwordx4 v136, s[26:27]
	s_mov_b32 m0, s36
	s_nop 0
	global_load_lds_dwordx4 v132, s[26:27]
	s_waitcnt vmcnt(8)
	s_waitcnt lgkmcnt(0)
	s_barrier
	s_setprio 1
	s_waitcnt lgkmcnt(0)
	v_mfma_f32_16x16x32_bf16 v[62:65], v[146:149], v[184:187], v[62:65]
	v_mfma_f32_16x16x32_bf16 v[58:61], v[160:163], v[184:187], v[58:61]
	v_mfma_f32_16x16x32_bf16 v[46:49], v[146:149], v[192:195], v[46:49]
	v_mfma_f32_16x16x32_bf16 v[42:45], v[160:163], v[192:195], v[42:45]
	v_mfma_f32_16x16x32_bf16 v[30:33], v[146:149], v[200:203], v[30:33]
	v_mfma_f32_16x16x32_bf16 v[26:29], v[160:163], v[200:203], v[26:29]
	v_mfma_f32_16x16x32_bf16 v[14:17], v[146:149], v[208:211], v[14:17]
	v_mfma_f32_16x16x32_bf16 v[10:13], v[160:163], v[208:211], v[10:13]
	v_mfma_f32_16x16x32_bf16 v[62:65], v[156:159], v[188:191], v[62:65]
	v_mfma_f32_16x16x32_bf16 v[58:61], v[164:167], v[188:191], v[58:61]
	v_mfma_f32_16x16x32_bf16 v[46:49], v[156:159], v[196:199], v[46:49]
	v_mfma_f32_16x16x32_bf16 v[42:45], v[164:167], v[196:199], v[42:45]
	v_mfma_f32_16x16x32_bf16 v[30:33], v[156:159], v[204:207], v[30:33]
	v_mfma_f32_16x16x32_bf16 v[26:29], v[164:167], v[204:207], v[26:29]
	v_mfma_f32_16x16x32_bf16 v[14:17], v[156:159], v[212:215], v[14:17]
	v_mfma_f32_16x16x32_bf16 v[10:13], v[164:167], v[212:215], v[10:13]
	s_setprio 0
	s_setprio 1
	v_mfma_f32_16x16x32_bf16 v[54:57], v[168:171], v[184:187], v[54:57]
	v_mfma_f32_16x16x32_bf16 v[50:53], v[176:179], v[184:187], v[50:53]
	v_mfma_f32_16x16x32_bf16 v[38:41], v[168:171], v[192:195], v[38:41]
	v_mfma_f32_16x16x32_bf16 v[34:37], v[176:179], v[192:195], v[34:37]
	v_mfma_f32_16x16x32_bf16 v[22:25], v[168:171], v[200:203], v[22:25]
	v_mfma_f32_16x16x32_bf16 v[18:21], v[176:179], v[200:203], v[18:21]
	v_mfma_f32_16x16x32_bf16 v[6:9], v[168:171], v[208:211], v[6:9]
	v_mfma_f32_16x16x32_bf16 v[2:5], v[176:179], v[208:211], v[2:5]
	v_mfma_f32_16x16x32_bf16 v[54:57], v[172:175], v[188:191], v[54:57]
	v_mfma_f32_16x16x32_bf16 v[50:53], v[180:183], v[188:191], v[50:53]
	v_mfma_f32_16x16x32_bf16 v[38:41], v[172:175], v[196:199], v[38:41]
	v_mfma_f32_16x16x32_bf16 v[34:37], v[180:183], v[196:199], v[34:37]
	v_mfma_f32_16x16x32_bf16 v[22:25], v[172:175], v[204:207], v[22:25]
	v_mfma_f32_16x16x32_bf16 v[18:21], v[180:183], v[204:207], v[18:21]
	v_mfma_f32_16x16x32_bf16 v[6:9], v[172:175], v[212:215], v[6:9]
	v_mfma_f32_16x16x32_bf16 v[2:5], v[180:183], v[212:215], v[2:5]
	s_setprio 0
	s_barrier
	s_add_i32 s70, 0, 0x18000
	v_add_u32_e32 v155, s70, v150
	s_add_i32 s71, 0, 0x1c000
	ds_read_b128 v[146:149], v155
	ds_read_b128 v[156:159], v155 offset:1024
	ds_read_b128 v[160:163], v155 offset:2048
	ds_read_b128 v[164:167], v155 offset:3072
	v_add_u32_e32 v155, s71, v150
	ds_read_b128 v[168:171], v155
	ds_read_b128 v[172:175], v155 offset:1024
	ds_read_b128 v[176:179], v155 offset:2048
	ds_read_b128 v[180:183], v155 offset:3072
	s_add_u32 s26, s26, 0x80000
	s_addc_u32 s27, s27, 0
	s_mov_b32 m0, s37
	ds_read_b128 v[184:187], v154 offset:32768
	ds_read_b128 v[188:191], v154 offset:33792
	ds_read_b128 v[192:195], v154 offset:34816
	ds_read_b128 v[196:199], v154 offset:35840
	ds_read_b128 v[200:203], v154 offset:36864
	ds_read_b128 v[204:207], v154 offset:37888
	ds_read_b128 v[208:211], v154 offset:38912
	ds_read_b128 v[212:215], v154 offset:39936
	global_load_lds_dwordx4 v136, s[26:27]
	s_mov_b32 m0, s42
	s_nop 0
	global_load_lds_dwordx4 v132, s[26:27]
	s_waitcnt vmcnt(8)
	s_waitcnt lgkmcnt(0)
	s_barrier
	s_setprio 1
	s_waitcnt lgkmcnt(0)
	v_mfma_f32_16x16x32_bf16 v[126:129], v[146:149], v[184:187], v[126:129]
	v_mfma_f32_16x16x32_bf16 v[122:125], v[160:163], v[184:187], v[122:125]
	v_mfma_f32_16x16x32_bf16 v[110:113], v[146:149], v[192:195], v[110:113]
	v_mfma_f32_16x16x32_bf16 v[106:109], v[160:163], v[192:195], v[106:109]
	v_mfma_f32_16x16x32_bf16 v[94:97], v[146:149], v[200:203], v[94:97]
	v_mfma_f32_16x16x32_bf16 v[90:93], v[160:163], v[200:203], v[90:93]
	v_mfma_f32_16x16x32_bf16 v[78:81], v[146:149], v[208:211], v[78:81]
	v_mfma_f32_16x16x32_bf16 v[74:77], v[160:163], v[208:211], v[74:77]
	v_mfma_f32_16x16x32_bf16 v[126:129], v[156:159], v[188:191], v[126:129]
	v_mfma_f32_16x16x32_bf16 v[122:125], v[164:167], v[188:191], v[122:125]
	v_mfma_f32_16x16x32_bf16 v[110:113], v[156:159], v[196:199], v[110:113]
	v_mfma_f32_16x16x32_bf16 v[106:109], v[164:167], v[196:199], v[106:109]
	v_mfma_f32_16x16x32_bf16 v[94:97], v[156:159], v[204:207], v[94:97]
	v_mfma_f32_16x16x32_bf16 v[90:93], v[164:167], v[204:207], v[90:93]
	v_mfma_f32_16x16x32_bf16 v[78:81], v[156:159], v[212:215], v[78:81]
	v_mfma_f32_16x16x32_bf16 v[74:77], v[164:167], v[212:215], v[74:77]
	s_setprio 0
	s_setprio 1
	v_mfma_f32_16x16x32_bf16 v[118:121], v[168:171], v[184:187], v[118:121]
	v_mfma_f32_16x16x32_bf16 v[114:117], v[176:179], v[184:187], v[114:117]
	v_mfma_f32_16x16x32_bf16 v[102:105], v[168:171], v[192:195], v[102:105]
	v_mfma_f32_16x16x32_bf16 v[98:101], v[176:179], v[192:195], v[98:101]
	v_mfma_f32_16x16x32_bf16 v[86:89], v[168:171], v[200:203], v[86:89]
	v_mfma_f32_16x16x32_bf16 v[82:85], v[176:179], v[200:203], v[82:85]
	v_mfma_f32_16x16x32_bf16 v[70:73], v[168:171], v[208:211], v[70:73]
	v_mfma_f32_16x16x32_bf16 v[66:69], v[176:179], v[208:211], v[66:69]
	v_mfma_f32_16x16x32_bf16 v[118:121], v[172:175], v[188:191], v[118:121]
	v_mfma_f32_16x16x32_bf16 v[114:117], v[180:183], v[188:191], v[114:117]
	v_mfma_f32_16x16x32_bf16 v[102:105], v[172:175], v[196:199], v[102:105]
	v_mfma_f32_16x16x32_bf16 v[98:101], v[180:183], v[196:199], v[98:101]
	v_mfma_f32_16x16x32_bf16 v[86:89], v[172:175], v[204:207], v[86:89]
	v_mfma_f32_16x16x32_bf16 v[82:85], v[180:183], v[204:207], v[82:85]
	v_mfma_f32_16x16x32_bf16 v[70:73], v[172:175], v[212:215], v[70:73]
	v_mfma_f32_16x16x32_bf16 v[66:69], v[180:183], v[212:215], v[66:69]
	s_setprio 0
	s_barrier
	s_add_i32 s26, s70, s33
	v_lshl_add_u64 v[216:217], v[216:217], 0, s[8:9]
	s_mov_b32 m0, s26
	ds_read_b128 v[184:187], v154 offset:49152
	ds_read_b128 v[188:191], v154 offset:50176
	ds_read_b128 v[192:195], v154 offset:51200
	ds_read_b128 v[196:199], v154 offset:52224
	ds_read_b128 v[200:203], v154 offset:53248
	ds_read_b128 v[204:207], v154 offset:54272
	ds_read_b128 v[208:211], v154 offset:55296
	ds_read_b128 v[212:215], v154 offset:56320
	global_load_lds_dwordx4 v[216:217], off
	s_add_i32 m0, s26, 0x2000
	s_add_u32 s24, s24, 0x80080
	v_lshl_add_u64 v[216:217], v[218:219], 0, s[8:9]
	s_addc_u32 s25, s25, 0
	s_add_i32 s26, s71, s33
	global_load_lds_dwordx4 v[216:217], off
	s_mov_b32 m0, s26
	s_nop 0
	global_load_lds_dwordx4 v134, s[24:25]
	s_add_i32 m0, s26, 0x2000
	s_nop 0
	global_load_lds_dwordx4 v130, s[24:25]
	v_lshl_add_u64 v[216:217], v[220:221], 0, s[8:9]
	s_mov_b32 m0, s44
	s_nop 0
	global_load_lds_dwordx4 v[216:217], off
	v_lshl_add_u64 v[216:217], v[222:223], 0, s[8:9]
	s_mov_b32 m0, s45
	s_nop 0
	global_load_lds_dwordx4 v[216:217], off
	s_waitcnt vmcnt(8)
	s_waitcnt lgkmcnt(0)
	s_barrier
	s_setprio 1
	s_waitcnt lgkmcnt(0)
	v_mfma_f32_16x16x32_bf16 v[62:65], v[146:149], v[184:187], v[62:65]
	v_mfma_f32_16x16x32_bf16 v[58:61], v[160:163], v[184:187], v[58:61]
	v_mfma_f32_16x16x32_bf16 v[46:49], v[146:149], v[192:195], v[46:49]
	v_mfma_f32_16x16x32_bf16 v[42:45], v[160:163], v[192:195], v[42:45]
	v_mfma_f32_16x16x32_bf16 v[30:33], v[146:149], v[200:203], v[30:33]
	v_mfma_f32_16x16x32_bf16 v[26:29], v[160:163], v[200:203], v[26:29]
	v_mfma_f32_16x16x32_bf16 v[14:17], v[146:149], v[208:211], v[14:17]
	v_mfma_f32_16x16x32_bf16 v[10:13], v[160:163], v[208:211], v[10:13]
	v_mfma_f32_16x16x32_bf16 v[62:65], v[156:159], v[188:191], v[62:65]
	v_mfma_f32_16x16x32_bf16 v[58:61], v[164:167], v[188:191], v[58:61]
	v_mfma_f32_16x16x32_bf16 v[46:49], v[156:159], v[196:199], v[46:49]
	v_mfma_f32_16x16x32_bf16 v[42:45], v[164:167], v[196:199], v[42:45]
	v_mfma_f32_16x16x32_bf16 v[30:33], v[156:159], v[204:207], v[30:33]
	v_mfma_f32_16x16x32_bf16 v[26:29], v[164:167], v[204:207], v[26:29]
	v_mfma_f32_16x16x32_bf16 v[14:17], v[156:159], v[212:215], v[14:17]
	v_mfma_f32_16x16x32_bf16 v[10:13], v[164:167], v[212:215], v[10:13]
	s_setprio 0
	s_setprio 1
	v_mfma_f32_16x16x32_bf16 v[54:57], v[168:171], v[184:187], v[54:57]
	v_mfma_f32_16x16x32_bf16 v[50:53], v[176:179], v[184:187], v[50:53]
	v_mfma_f32_16x16x32_bf16 v[38:41], v[168:171], v[192:195], v[38:41]
	v_mfma_f32_16x16x32_bf16 v[34:37], v[176:179], v[192:195], v[34:37]
	v_mfma_f32_16x16x32_bf16 v[22:25], v[168:171], v[200:203], v[22:25]
	v_mfma_f32_16x16x32_bf16 v[18:21], v[176:179], v[200:203], v[18:21]
	v_mfma_f32_16x16x32_bf16 v[6:9], v[168:171], v[208:211], v[6:9]
	v_mfma_f32_16x16x32_bf16 v[2:5], v[176:179], v[208:211], v[2:5]
	v_mfma_f32_16x16x32_bf16 v[54:57], v[172:175], v[188:191], v[54:57]
	v_mfma_f32_16x16x32_bf16 v[50:53], v[180:183], v[188:191], v[50:53]
	v_mfma_f32_16x16x32_bf16 v[38:41], v[172:175], v[196:199], v[38:41]
	v_mfma_f32_16x16x32_bf16 v[34:37], v[180:183], v[196:199], v[34:37]
	v_mfma_f32_16x16x32_bf16 v[22:25], v[172:175], v[204:207], v[22:25]
	v_mfma_f32_16x16x32_bf16 v[18:21], v[180:183], v[204:207], v[18:21]
	v_mfma_f32_16x16x32_bf16 v[6:9], v[172:175], v[212:215], v[6:9]
	v_mfma_f32_16x16x32_bf16 v[2:5], v[180:183], v[212:215], v[2:5]
	s_setprio 0
	s_barrier
	s_add_i32 s69, s69, 2
	s_add_u32 s22, s22, 0x100
	s_addc_u32 s23, s23, 0
	s_add_u32 s67, s67, 0x100
	s_addc_u32 s68, s68, 0
	s_cmp_gt_u32 s69, 29
	s_cbranch_scc0 .LBB0_574
	s_and_b64 vcc, exec, s[10:11]
	s_cbranch_vccz .LBB0_577
	s_barrier

.LBB0_659:
	ds_read_b128 v[150:153], v211
	ds_read_b128 v[154:157], v211 offset:1024
	ds_read_b128 v[158:161], v211 offset:2048
	ds_read_b128 v[162:165], v211 offset:3072
	ds_read_b128 v[166:169], v212
	ds_read_b128 v[170:173], v212 offset:1024
	ds_read_b128 v[174:177], v212 offset:2048
	ds_read_b128 v[178:181], v212 offset:3072
	s_add_u32 s36, s0, 0xffea8080
	s_addc_u32 s37, s1, -1
	s_cmpk_eq_i32 s44, 0x52
	s_cselect_b32 s43, s27, s37
	s_cselect_b32 s42, s26, s36
	s_cselect_b32 s37, s29, s35
	s_cselect_b32 s36, s28, s31
	s_add_i32 m0, s63, 0xc000
	ds_read_b128 v[182:185], v213
	ds_read_b128 v[186:189], v213 offset:1024
	ds_read_b128 v[190:193], v213 offset:2048
	ds_read_b128 v[194:197], v213 offset:3072
	ds_read_b128 v[198:201], v213 offset:4096
	ds_read_b128 v[202:205], v213 offset:5120
	ds_read_b128 v[218:221], v213 offset:6144
	ds_read_b128 v[222:225], v213 offset:7168
	global_load_lds_dwordx4 v142, s[0:1]
	s_add_i32 m0, s63, 0xe000
	s_nop 0
	global_load_lds_dwordx4 v144, s[0:1]
	s_waitcnt vmcnt(8)
	s_waitcnt lgkmcnt(0)
	s_barrier
	s_setprio 1
	s_waitcnt lgkmcnt(0)
	v_mfma_f32_16x16x32_bf16 v[126:129], v[150:153], v[182:185], v[126:129]
	v_mfma_f32_16x16x32_bf16 v[122:125], v[158:161], v[182:185], v[122:125]
	v_mfma_f32_16x16x32_bf16 v[110:113], v[150:153], v[190:193], v[110:113]
	v_mfma_f32_16x16x32_bf16 v[106:109], v[158:161], v[190:193], v[106:109]
	v_mfma_f32_16x16x32_bf16 v[94:97], v[150:153], v[198:201], v[94:97]
	v_mfma_f32_16x16x32_bf16 v[90:93], v[158:161], v[198:201], v[90:93]
	v_mfma_f32_16x16x32_bf16 v[78:81], v[150:153], v[218:221], v[78:81]
	v_mfma_f32_16x16x32_bf16 v[74:77], v[158:161], v[218:221], v[74:77]
	v_mfma_f32_16x16x32_bf16 v[126:129], v[154:157], v[186:189], v[126:129]
	v_mfma_f32_16x16x32_bf16 v[122:125], v[162:165], v[186:189], v[122:125]
	v_mfma_f32_16x16x32_bf16 v[110:113], v[154:157], v[194:197], v[110:113]
	v_mfma_f32_16x16x32_bf16 v[106:109], v[162:165], v[194:197], v[106:109]
	v_mfma_f32_16x16x32_bf16 v[94:97], v[154:157], v[202:205], v[94:97]
	v_mfma_f32_16x16x32_bf16 v[90:93], v[162:165], v[202:205], v[90:93]
	v_mfma_f32_16x16x32_bf16 v[78:81], v[154:157], v[222:225], v[78:81]
	v_mfma_f32_16x16x32_bf16 v[74:77], v[162:165], v[222:225], v[74:77]
	s_setprio 0
	s_setprio 1
	v_mfma_f32_16x16x32_bf16 v[118:121], v[166:169], v[182:185], v[118:121]
	v_mfma_f32_16x16x32_bf16 v[114:117], v[174:177], v[182:185], v[114:117]
	v_mfma_f32_16x16x32_bf16 v[102:105], v[166:169], v[190:193], v[102:105]
	v_mfma_f32_16x16x32_bf16 v[98:101], v[174:177], v[190:193], v[98:101]
	v_mfma_f32_16x16x32_bf16 v[86:89], v[166:169], v[198:201], v[86:89]
	v_mfma_f32_16x16x32_bf16 v[82:85], v[174:177], v[198:201], v[82:85]
	v_mfma_f32_16x16x32_bf16 v[70:73], v[166:169], v[218:221], v[70:73]
	v_mfma_f32_16x16x32_bf16 v[66:69], v[174:177], v[218:221], v[66:69]
	v_mfma_f32_16x16x32_bf16 v[118:121], v[170:173], v[186:189], v[118:121]
	v_mfma_f32_16x16x32_bf16 v[114:117], v[178:181], v[186:189], v[114:117]
	v_mfma_f32_16x16x32_bf16 v[102:105], v[170:173], v[194:197], v[102:105]
	v_mfma_f32_16x16x32_bf16 v[98:101], v[178:181], v[194:197], v[98:101]
	v_mfma_f32_16x16x32_bf16 v[86:89], v[170:173], v[202:205], v[86:89]
	v_mfma_f32_16x16x32_bf16 v[82:85], v[178:181], v[202:205], v[82:85]
	v_mfma_f32_16x16x32_bf16 v[70:73], v[170:173], v[222:225], v[70:73]
	v_mfma_f32_16x16x32_bf16 v[66:69], v[178:181], v[222:225], v[66:69]
	s_setprio 0
	s_barrier
	s_add_i32 s45, s75, s62
	v_lshl_add_u64 v[226:227], s[36:37], 0, v[132:133]
	s_mov_b32 m0, s45
	ds_read_b128 v[182:185], v213 offset:16384
	ds_read_b128 v[186:189], v213 offset:17408
	ds_read_b128 v[190:193], v213 offset:18432
	ds_read_b128 v[194:197], v213 offset:19456
	ds_read_b128 v[198:201], v213 offset:20480
	ds_read_b128 v[202:205], v213 offset:21504
	ds_read_b128 v[218:221], v213 offset:22528
	ds_read_b128 v[222:225], v213 offset:23552
	global_load_lds_dwordx4 v132, s[36:37]
	s_add_i32 m0, s45, 0x2000
	s_add_u32 s82, s36, 0x158000
	v_lshl_add_u64 v[228:229], s[36:37], 0, v[136:137]
	s_addc_u32 s83, s37, 0
	s_add_i32 s45, s76, s62
	global_load_lds_dwordx4 v136, s[36:37]
	s_mov_b32 m0, s45
	v_lshl_add_u64 v[232:233], s[42:43], 0, v[134:135]
	global_load_lds_dwordx4 v132, s[82:83]
	s_add_i32 m0, s45, 0x2000
	s_nop 0
	global_load_lds_dwordx4 v136, s[82:83]
	v_lshl_add_u64 v[230:231], s[42:43], 0, v[130:131]
	s_mov_b32 m0, s63
	s_nop 0
	global_load_lds_dwordx4 v130, s[42:43]
	s_mov_b32 m0, s64
	s_nop 0
	global_load_lds_dwordx4 v134, s[42:43]
	s_waitcnt vmcnt(8)
	s_waitcnt lgkmcnt(0)
	s_barrier
	s_setprio 1
	s_waitcnt lgkmcnt(0)
	v_mfma_f32_16x16x32_bf16 v[62:65], v[150:153], v[182:185], v[62:65]
	v_mfma_f32_16x16x32_bf16 v[58:61], v[158:161], v[182:185], v[58:61]
	v_mfma_f32_16x16x32_bf16 v[46:49], v[150:153], v[190:193], v[46:49]
	v_mfma_f32_16x16x32_bf16 v[42:45], v[158:161], v[190:193], v[42:45]
	v_mfma_f32_16x16x32_bf16 v[30:33], v[150:153], v[198:201], v[30:33]
	v_mfma_f32_16x16x32_bf16 v[26:29], v[158:161], v[198:201], v[26:29]
	v_mfma_f32_16x16x32_bf16 v[14:17], v[150:153], v[218:221], v[14:17]
	v_mfma_f32_16x16x32_bf16 v[10:13], v[158:161], v[218:221], v[10:13]
	v_mfma_f32_16x16x32_bf16 v[62:65], v[154:157], v[186:189], v[62:65]
	v_mfma_f32_16x16x32_bf16 v[58:61], v[162:165], v[186:189], v[58:61]
	v_mfma_f32_16x16x32_bf16 v[46:49], v[154:157], v[194:197], v[46:49]
	v_mfma_f32_16x16x32_bf16 v[42:45], v[162:165], v[194:197], v[42:45]
	v_mfma_f32_16x16x32_bf16 v[30:33], v[154:157], v[202:205], v[30:33]
	v_mfma_f32_16x16x32_bf16 v[26:29], v[162:165], v[202:205], v[26:29]
	v_mfma_f32_16x16x32_bf16 v[14:17], v[154:157], v[222:225], v[14:17]
	v_mfma_f32_16x16x32_bf16 v[10:13], v[162:165], v[222:225], v[10:13]
	s_setprio 0
	s_setprio 1
	v_mfma_f32_16x16x32_bf16 v[54:57], v[166:169], v[182:185], v[54:57]
	v_mfma_f32_16x16x32_bf16 v[50:53], v[174:177], v[182:185], v[50:53]
	v_mfma_f32_16x16x32_bf16 v[38:41], v[166:169], v[190:193], v[38:41]
	v_mfma_f32_16x16x32_bf16 v[34:37], v[174:177], v[190:193], v[34:37]
	v_mfma_f32_16x16x32_bf16 v[22:25], v[166:169], v[198:201], v[22:25]
	v_mfma_f32_16x16x32_bf16 v[18:21], v[174:177], v[198:201], v[18:21]
	v_mfma_f32_16x16x32_bf16 v[6:9], v[166:169], v[218:221], v[6:9]
	v_mfma_f32_16x16x32_bf16 v[2:5], v[174:177], v[218:221], v[2:5]
	v_mfma_f32_16x16x32_bf16 v[54:57], v[170:173], v[186:189], v[54:57]
	v_mfma_f32_16x16x32_bf16 v[50:53], v[178:181], v[186:189], v[50:53]
	v_mfma_f32_16x16x32_bf16 v[38:41], v[170:173], v[194:197], v[38:41]
	v_mfma_f32_16x16x32_bf16 v[34:37], v[178:181], v[194:197], v[34:37]
	v_mfma_f32_16x16x32_bf16 v[22:25], v[170:173], v[202:205], v[22:25]
	v_mfma_f32_16x16x32_bf16 v[18:21], v[178:181], v[202:205], v[18:21]
	v_mfma_f32_16x16x32_bf16 v[6:9], v[170:173], v[222:225], v[6:9]
	v_mfma_f32_16x16x32_bf16 v[2:5], v[178:181], v[222:225], v[2:5]
	s_setprio 0
	s_barrier
	s_add_i32 s45, 0, 0x18000
	v_add_u32_e32 v139, s45, v206
	s_add_i32 s81, 0, 0x1c000
	ds_read_b128 v[150:153], v139
	ds_read_b128 v[154:157], v139 offset:1024
	ds_read_b128 v[158:161], v139 offset:2048
	ds_read_b128 v[162:165], v139 offset:3072
	v_add_u32_e32 v139, s81, v206
	ds_read_b128 v[166:169], v139
	ds_read_b128 v[170:173], v139 offset:1024
	ds_read_b128 v[174:177], v139 offset:2048
	ds_read_b128 v[178:181], v139 offset:3072
	s_add_u32 s42, s42, 0x158000
	s_addc_u32 s43, s43, 0
	s_mov_b32 m0, s65
	ds_read_b128 v[182:185], v213 offset:32768
	ds_read_b128 v[186:189], v213 offset:33792
	ds_read_b128 v[190:193], v213 offset:34816
	ds_read_b128 v[194:197], v213 offset:35840
	ds_read_b128 v[198:201], v213 offset:36864
	ds_read_b128 v[202:205], v213 offset:37888
	ds_read_b128 v[218:221], v213 offset:38912
	ds_read_b128 v[222:225], v213 offset:39936
	global_load_lds_dwordx4 v130, s[42:43]
	s_mov_b32 m0, s66
	s_nop 0
	global_load_lds_dwordx4 v134, s[42:43]
	s_waitcnt vmcnt(8)
	s_waitcnt lgkmcnt(0)
	s_barrier
	s_setprio 1
	s_waitcnt lgkmcnt(0)
	v_mfma_f32_16x16x32_bf16 v[126:129], v[150:153], v[182:185], v[126:129]
	v_mfma_f32_16x16x32_bf16 v[122:125], v[158:161], v[182:185], v[122:125]
	v_mfma_f32_16x16x32_bf16 v[110:113], v[150:153], v[190:193], v[110:113]
	v_mfma_f32_16x16x32_bf16 v[106:109], v[158:161], v[190:193], v[106:109]
	v_mfma_f32_16x16x32_bf16 v[94:97], v[150:153], v[198:201], v[94:97]
	v_mfma_f32_16x16x32_bf16 v[90:93], v[158:161], v[198:201], v[90:93]
	v_mfma_f32_16x16x32_bf16 v[78:81], v[150:153], v[218:221], v[78:81]
	v_mfma_f32_16x16x32_bf16 v[74:77], v[158:161], v[218:221], v[74:77]
	v_mfma_f32_16x16x32_bf16 v[126:129], v[154:157], v[186:189], v[126:129]
	v_mfma_f32_16x16x32_bf16 v[122:125], v[162:165], v[186:189], v[122:125]
	v_mfma_f32_16x16x32_bf16 v[110:113], v[154:157], v[194:197], v[110:113]
	v_mfma_f32_16x16x32_bf16 v[106:109], v[162:165], v[194:197], v[106:109]
	v_mfma_f32_16x16x32_bf16 v[94:97], v[154:157], v[202:205], v[94:97]
	v_mfma_f32_16x16x32_bf16 v[90:93], v[162:165], v[202:205], v[90:93]
	v_mfma_f32_16x16x32_bf16 v[78:81], v[154:157], v[222:225], v[78:81]
	v_mfma_f32_16x16x32_bf16 v[74:77], v[162:165], v[222:225], v[74:77]
	s_setprio 0
	s_setprio 1
	v_mfma_f32_16x16x32_bf16 v[118:121], v[166:169], v[182:185], v[118:121]
	v_mfma_f32_16x16x32_bf16 v[114:117], v[174:177], v[182:185], v[114:117]
	v_mfma_f32_16x16x32_bf16 v[102:105], v[166:169], v[190:193], v[102:105]
	v_mfma_f32_16x16x32_bf16 v[98:101], v[174:177], v[190:193], v[98:101]
	v_mfma_f32_16x16x32_bf16 v[86:89], v[166:169], v[198:201], v[86:89]
	v_mfma_f32_16x16x32_bf16 v[82:85], v[174:177], v[198:201], v[82:85]
	v_mfma_f32_16x16x32_bf16 v[70:73], v[166:169], v[218:221], v[70:73]
	v_mfma_f32_16x16x32_bf16 v[66:69], v[174:177], v[218:221], v[66:69]
	v_mfma_f32_16x16x32_bf16 v[118:121], v[170:173], v[186:189], v[118:121]
	v_mfma_f32_16x16x32_bf16 v[114:117], v[178:181], v[186:189], v[114:117]
	v_mfma_f32_16x16x32_bf16 v[102:105], v[170:173], v[194:197], v[102:105]
	v_mfma_f32_16x16x32_bf16 v[98:101], v[178:181], v[194:197], v[98:101]
	v_mfma_f32_16x16x32_bf16 v[86:89], v[170:173], v[202:205], v[86:89]
	v_mfma_f32_16x16x32_bf16 v[82:85], v[178:181], v[202:205], v[82:85]
	v_mfma_f32_16x16x32_bf16 v[70:73], v[170:173], v[222:225], v[70:73]
	v_mfma_f32_16x16x32_bf16 v[66:69], v[178:181], v[222:225], v[66:69]
	s_setprio 0
	s_barrier
	s_add_i32 s42, s45, s62
	v_lshl_add_u64 v[226:227], v[226:227], 0, s[20:21]
	s_mov_b32 m0, s42
	ds_read_b128 v[182:185], v213 offset:49152
	ds_read_b128 v[186:189], v213 offset:50176
	ds_read_b128 v[190:193], v213 offset:51200
	ds_read_b128 v[194:197], v213 offset:52224
	ds_read_b128 v[198:201], v213 offset:53248
	ds_read_b128 v[202:205], v213 offset:54272
	ds_read_b128 v[218:221], v213 offset:55296
	ds_read_b128 v[222:225], v213 offset:56320
	global_load_lds_dwordx4 v[226:227], off
	s_add_i32 m0, s42, 0x2000
	s_add_u32 s36, s36, 0x158080
	v_lshl_add_u64 v[226:227], v[228:229], 0, s[20:21]
	s_addc_u32 s37, s37, 0
	s_add_i32 s42, s81, s62
	global_load_lds_dwordx4 v[226:227], off
	s_mov_b32 m0, s42
	s_nop 0
	global_load_lds_dwordx4 v132, s[36:37]
	s_add_i32 m0, s42, 0x2000
	s_nop 0
	global_load_lds_dwordx4 v136, s[36:37]
	v_lshl_add_u64 v[226:227], v[230:231], 0, s[20:21]
	s_mov_b32 m0, s70
	s_nop 0
	global_load_lds_dwordx4 v[226:227], off
	v_lshl_add_u64 v[226:227], v[232:233], 0, s[20:21]
	s_mov_b32 m0, s71
	s_nop 0
	global_load_lds_dwordx4 v[226:227], off
	s_waitcnt vmcnt(8)
	s_waitcnt lgkmcnt(0)
	s_barrier
	s_setprio 1
	s_waitcnt lgkmcnt(0)
	v_mfma_f32_16x16x32_bf16 v[62:65], v[150:153], v[182:185], v[62:65]
	v_mfma_f32_16x16x32_bf16 v[58:61], v[158:161], v[182:185], v[58:61]
	v_mfma_f32_16x16x32_bf16 v[46:49], v[150:153], v[190:193], v[46:49]
	v_mfma_f32_16x16x32_bf16 v[42:45], v[158:161], v[190:193], v[42:45]
	v_mfma_f32_16x16x32_bf16 v[30:33], v[150:153], v[198:201], v[30:33]
	v_mfma_f32_16x16x32_bf16 v[26:29], v[158:161], v[198:201], v[26:29]
	v_mfma_f32_16x16x32_bf16 v[14:17], v[150:153], v[218:221], v[14:17]
	v_mfma_f32_16x16x32_bf16 v[10:13], v[158:161], v[218:221], v[10:13]
	v_mfma_f32_16x16x32_bf16 v[62:65], v[154:157], v[186:189], v[62:65]
	v_mfma_f32_16x16x32_bf16 v[58:61], v[162:165], v[186:189], v[58:61]
	v_mfma_f32_16x16x32_bf16 v[46:49], v[154:157], v[194:197], v[46:49]
	v_mfma_f32_16x16x32_bf16 v[42:45], v[162:165], v[194:197], v[42:45]
	v_mfma_f32_16x16x32_bf16 v[30:33], v[154:157], v[202:205], v[30:33]
	v_mfma_f32_16x16x32_bf16 v[26:29], v[162:165], v[202:205], v[26:29]
	v_mfma_f32_16x16x32_bf16 v[14:17], v[154:157], v[222:225], v[14:17]
	v_mfma_f32_16x16x32_bf16 v[10:13], v[162:165], v[222:225], v[10:13]
	s_setprio 0
	s_setprio 1
	v_mfma_f32_16x16x32_bf16 v[54:57], v[166:169], v[182:185], v[54:57]
	v_mfma_f32_16x16x32_bf16 v[50:53], v[174:177], v[182:185], v[50:53]
	v_mfma_f32_16x16x32_bf16 v[38:41], v[166:169], v[190:193], v[38:41]
	v_mfma_f32_16x16x32_bf16 v[34:37], v[174:177], v[190:193], v[34:37]
	v_mfma_f32_16x16x32_bf16 v[22:25], v[166:169], v[198:201], v[22:25]
	v_mfma_f32_16x16x32_bf16 v[18:21], v[174:177], v[198:201], v[18:21]
	v_mfma_f32_16x16x32_bf16 v[6:9], v[166:169], v[218:221], v[6:9]
	v_mfma_f32_16x16x32_bf16 v[2:5], v[174:177], v[218:221], v[2:5]
	v_mfma_f32_16x16x32_bf16 v[54:57], v[170:173], v[186:189], v[54:57]
	v_mfma_f32_16x16x32_bf16 v[50:53], v[178:181], v[186:189], v[50:53]
	v_mfma_f32_16x16x32_bf16 v[38:41], v[170:173], v[194:197], v[38:41]
	v_mfma_f32_16x16x32_bf16 v[34:37], v[178:181], v[194:197], v[34:37]
	v_mfma_f32_16x16x32_bf16 v[22:25], v[170:173], v[202:205], v[22:25]
	v_mfma_f32_16x16x32_bf16 v[18:21], v[178:181], v[202:205], v[18:21]
	v_mfma_f32_16x16x32_bf16 v[6:9], v[170:173], v[222:225], v[6:9]
	v_mfma_f32_16x16x32_bf16 v[2:5], v[178:181], v[222:225], v[2:5]
	s_setprio 0
	s_barrier
	s_add_i32 s44, s44, 2
	s_add_u32 s0, s0, 0x100
	s_addc_u32 s1, s1, 0
	s_add_u32 s31, s31, 0x100
	s_addc_u32 s35, s35, 0
	s_cmpk_gt_u32 s44, 0x53
	s_cbranch_scc0 .LBB0_659
	s_and_b64 vcc, exec, s[22:23]
	s_cbranch_vccz .LBB0_662
	s_barrier

.LBB0_767:
	ds_read_b128 v[146:149], v152
	ds_read_b128 v[156:159], v152 offset:1024
	ds_read_b128 v[160:163], v152 offset:2048
	ds_read_b128 v[164:167], v152 offset:3072
	ds_read_b128 v[168:171], v153
	ds_read_b128 v[172:175], v153 offset:1024
	ds_read_b128 v[176:179], v153 offset:2048
	ds_read_b128 v[180:183], v153 offset:3072
	s_add_u32 s24, s22, 0xfff80080
	s_addc_u32 s25, s23, -1
	s_cmp_eq_u32 s69, 28
	s_cselect_b32 s27, s15, s25
	s_cselect_b32 s26, s65, s24
	s_cselect_b32 s25, s13, s68
	s_cselect_b32 s24, s66, s67
	s_add_i32 m0, s21, 0xc000
	ds_read_b128 v[184:187], v154
	ds_read_b128 v[188:191], v154 offset:1024
	ds_read_b128 v[192:195], v154 offset:2048
	ds_read_b128 v[196:199], v154 offset:3072
	ds_read_b128 v[200:203], v154 offset:4096
	ds_read_b128 v[204:207], v154 offset:5120
	ds_read_b128 v[208:211], v154 offset:6144
	ds_read_b128 v[212:215], v154 offset:7168
	global_load_lds_dwordx4 v138, s[22:23]
	s_add_i32 m0, s21, 0xe000
	s_nop 0
	global_load_lds_dwordx4 v140, s[22:23]
	s_waitcnt vmcnt(8)
	s_waitcnt lgkmcnt(0)
	s_barrier
	s_setprio 1
	s_waitcnt lgkmcnt(0)
	v_mfma_f32_16x16x32_bf16 v[126:129], v[146:149], v[184:187], v[126:129]
	v_mfma_f32_16x16x32_bf16 v[122:125], v[160:163], v[184:187], v[122:125]
	v_mfma_f32_16x16x32_bf16 v[118:121], v[146:149], v[192:195], v[118:121]
	v_mfma_f32_16x16x32_bf16 v[110:113], v[160:163], v[192:195], v[110:113]
	v_mfma_f32_16x16x32_bf16 v[102:105], v[146:149], v[200:203], v[102:105]
	v_mfma_f32_16x16x32_bf16 v[94:97], v[160:163], v[200:203], v[94:97]
	v_mfma_f32_16x16x32_bf16 v[86:89], v[146:149], v[208:211], v[86:89]
	v_mfma_f32_16x16x32_bf16 v[78:81], v[160:163], v[208:211], v[78:81]
	v_mfma_f32_16x16x32_bf16 v[126:129], v[156:159], v[188:191], v[126:129]
	v_mfma_f32_16x16x32_bf16 v[122:125], v[164:167], v[188:191], v[122:125]
	v_mfma_f32_16x16x32_bf16 v[118:121], v[156:159], v[196:199], v[118:121]
	v_mfma_f32_16x16x32_bf16 v[110:113], v[164:167], v[196:199], v[110:113]
	v_mfma_f32_16x16x32_bf16 v[102:105], v[156:159], v[204:207], v[102:105]
	v_mfma_f32_16x16x32_bf16 v[94:97], v[164:167], v[204:207], v[94:97]
	v_mfma_f32_16x16x32_bf16 v[86:89], v[156:159], v[212:215], v[86:89]
	v_mfma_f32_16x16x32_bf16 v[78:81], v[164:167], v[212:215], v[78:81]
	s_setprio 0
	s_setprio 1
	v_mfma_f32_16x16x32_bf16 v[114:117], v[168:171], v[184:187], v[114:117]
	v_mfma_f32_16x16x32_bf16 v[106:109], v[176:179], v[184:187], v[106:109]
	v_mfma_f32_16x16x32_bf16 v[98:101], v[168:171], v[192:195], v[98:101]
	v_mfma_f32_16x16x32_bf16 v[90:93], v[176:179], v[192:195], v[90:93]
	v_mfma_f32_16x16x32_bf16 v[82:85], v[168:171], v[200:203], v[82:85]
	v_mfma_f32_16x16x32_bf16 v[74:77], v[176:179], v[200:203], v[74:77]
	v_mfma_f32_16x16x32_bf16 v[70:73], v[168:171], v[208:211], v[70:73]
	v_mfma_f32_16x16x32_bf16 v[66:69], v[176:179], v[208:211], v[66:69]
	v_mfma_f32_16x16x32_bf16 v[114:117], v[172:175], v[188:191], v[114:117]
	v_mfma_f32_16x16x32_bf16 v[106:109], v[180:183], v[188:191], v[106:109]
	v_mfma_f32_16x16x32_bf16 v[98:101], v[172:175], v[196:199], v[98:101]
	v_mfma_f32_16x16x32_bf16 v[90:93], v[180:183], v[196:199], v[90:93]
	v_mfma_f32_16x16x32_bf16 v[82:85], v[172:175], v[204:207], v[82:85]
	v_mfma_f32_16x16x32_bf16 v[74:77], v[180:183], v[204:207], v[74:77]
	v_mfma_f32_16x16x32_bf16 v[70:73], v[172:175], v[212:215], v[70:73]
	v_mfma_f32_16x16x32_bf16 v[66:69], v[180:183], v[212:215], v[66:69]
	s_setprio 0
	s_barrier
	s_add_i32 s70, s61, s33
	v_lshl_add_u64 v[216:217], s[24:25], 0, v[134:135]
	s_mov_b32 m0, s70
	ds_read_b128 v[184:187], v154 offset:16384
	ds_read_b128 v[188:191], v154 offset:17408
	ds_read_b128 v[192:195], v154 offset:18432
	ds_read_b128 v[196:199], v154 offset:19456
	ds_read_b128 v[200:203], v154 offset:20480
	ds_read_b128 v[204:207], v154 offset:21504
	ds_read_b128 v[208:211], v154 offset:22528
	ds_read_b128 v[212:215], v154 offset:23552
	global_load_lds_dwordx4 v134, s[24:25]
	s_add_i32 m0, s70, 0x2000
	s_add_u32 s70, s24, 0x80000
	v_lshl_add_u64 v[218:219], s[24:25], 0, v[130:131]
	s_addc_u32 s71, s25, 0
	s_add_i32 s72, s62, s33
	global_load_lds_dwordx4 v130, s[24:25]
	s_mov_b32 m0, s72
	v_lshl_add_u64 v[222:223], s[26:27], 0, v[132:133]
	global_load_lds_dwordx4 v134, s[70:71]
	s_add_i32 m0, s72, 0x2000
	s_nop 0
	global_load_lds_dwordx4 v130, s[70:71]
	v_lshl_add_u64 v[220:221], s[26:27], 0, v[136:137]
	s_mov_b32 m0, s21
	s_nop 0
	global_load_lds_dwordx4 v136, s[26:27]
	s_mov_b32 m0, s36
	s_nop 0
	global_load_lds_dwordx4 v132, s[26:27]
	s_waitcnt vmcnt(8)
	s_waitcnt lgkmcnt(0)
	s_barrier
	s_setprio 1
	s_waitcnt lgkmcnt(0)
	v_mfma_f32_16x16x32_bf16 v[62:65], v[146:149], v[184:187], v[62:65]
	v_mfma_f32_16x16x32_bf16 v[58:61], v[160:163], v[184:187], v[58:61]
	v_mfma_f32_16x16x32_bf16 v[54:57], v[146:149], v[192:195], v[54:57]
	v_mfma_f32_16x16x32_bf16 v[46:49], v[160:163], v[192:195], v[46:49]
	v_mfma_f32_16x16x32_bf16 v[38:41], v[146:149], v[200:203], v[38:41]
	v_mfma_f32_16x16x32_bf16 v[30:33], v[160:163], v[200:203], v[30:33]
	v_mfma_f32_16x16x32_bf16 v[22:25], v[146:149], v[208:211], v[22:25]
	v_mfma_f32_16x16x32_bf16 v[14:17], v[160:163], v[208:211], v[14:17]
	v_mfma_f32_16x16x32_bf16 v[62:65], v[156:159], v[188:191], v[62:65]
	v_mfma_f32_16x16x32_bf16 v[58:61], v[164:167], v[188:191], v[58:61]
	v_mfma_f32_16x16x32_bf16 v[54:57], v[156:159], v[196:199], v[54:57]
	v_mfma_f32_16x16x32_bf16 v[46:49], v[164:167], v[196:199], v[46:49]
	v_mfma_f32_16x16x32_bf16 v[38:41], v[156:159], v[204:207], v[38:41]
	v_mfma_f32_16x16x32_bf16 v[30:33], v[164:167], v[204:207], v[30:33]
	v_mfma_f32_16x16x32_bf16 v[22:25], v[156:159], v[212:215], v[22:25]
	v_mfma_f32_16x16x32_bf16 v[14:17], v[164:167], v[212:215], v[14:17]
	s_setprio 0
	s_setprio 1
	v_mfma_f32_16x16x32_bf16 v[50:53], v[168:171], v[184:187], v[50:53]
	v_mfma_f32_16x16x32_bf16 v[42:45], v[176:179], v[184:187], v[42:45]
	v_mfma_f32_16x16x32_bf16 v[34:37], v[168:171], v[192:195], v[34:37]
	v_mfma_f32_16x16x32_bf16 v[26:29], v[176:179], v[192:195], v[26:29]
	v_mfma_f32_16x16x32_bf16 v[18:21], v[168:171], v[200:203], v[18:21]
	v_mfma_f32_16x16x32_bf16 v[10:13], v[176:179], v[200:203], v[10:13]
	v_mfma_f32_16x16x32_bf16 v[6:9], v[168:171], v[208:211], v[6:9]
	v_mfma_f32_16x16x32_bf16 v[2:5], v[176:179], v[208:211], v[2:5]
	v_mfma_f32_16x16x32_bf16 v[50:53], v[172:175], v[188:191], v[50:53]
	v_mfma_f32_16x16x32_bf16 v[42:45], v[180:183], v[188:191], v[42:45]
	v_mfma_f32_16x16x32_bf16 v[34:37], v[172:175], v[196:199], v[34:37]
	v_mfma_f32_16x16x32_bf16 v[26:29], v[180:183], v[196:199], v[26:29]
	v_mfma_f32_16x16x32_bf16 v[18:21], v[172:175], v[204:207], v[18:21]
	v_mfma_f32_16x16x32_bf16 v[10:13], v[180:183], v[204:207], v[10:13]
	v_mfma_f32_16x16x32_bf16 v[6:9], v[172:175], v[212:215], v[6:9]
	v_mfma_f32_16x16x32_bf16 v[2:5], v[180:183], v[212:215], v[2:5]
	s_setprio 0
	s_barrier
	s_add_i32 s70, 0, 0x18000
	v_add_u32_e32 v155, s70, v150
	s_add_i32 s71, 0, 0x1c000
	ds_read_b128 v[146:149], v155
	ds_read_b128 v[156:159], v155 offset:1024
	ds_read_b128 v[160:163], v155 offset:2048
	ds_read_b128 v[164:167], v155 offset:3072
	v_add_u32_e32 v155, s71, v150
	ds_read_b128 v[168:171], v155
	ds_read_b128 v[172:175], v155 offset:1024
	ds_read_b128 v[176:179], v155 offset:2048
	ds_read_b128 v[180:183], v155 offset:3072
	s_add_u32 s26, s26, 0x80000
	s_addc_u32 s27, s27, 0
	s_mov_b32 m0, s37
	ds_read_b128 v[184:187], v154 offset:32768
	ds_read_b128 v[188:191], v154 offset:33792
	ds_read_b128 v[192:195], v154 offset:34816
	ds_read_b128 v[196:199], v154 offset:35840
	ds_read_b128 v[200:203], v154 offset:36864
	ds_read_b128 v[204:207], v154 offset:37888
	ds_read_b128 v[208:211], v154 offset:38912
	ds_read_b128 v[212:215], v154 offset:39936
	global_load_lds_dwordx4 v136, s[26:27]
	s_mov_b32 m0, s42
	s_nop 0
	global_load_lds_dwordx4 v132, s[26:27]
	s_waitcnt vmcnt(8)
	s_waitcnt lgkmcnt(0)
	s_barrier
	s_setprio 1
	s_waitcnt lgkmcnt(0)
	v_mfma_f32_16x16x32_bf16 v[126:129], v[146:149], v[184:187], v[126:129]
	v_mfma_f32_16x16x32_bf16 v[122:125], v[160:163], v[184:187], v[122:125]
	v_mfma_f32_16x16x32_bf16 v[118:121], v[146:149], v[192:195], v[118:121]
	v_mfma_f32_16x16x32_bf16 v[110:113], v[160:163], v[192:195], v[110:113]
	v_mfma_f32_16x16x32_bf16 v[102:105], v[146:149], v[200:203], v[102:105]
	v_mfma_f32_16x16x32_bf16 v[94:97], v[160:163], v[200:203], v[94:97]
	v_mfma_f32_16x16x32_bf16 v[86:89], v[146:149], v[208:211], v[86:89]
	v_mfma_f32_16x16x32_bf16 v[78:81], v[160:163], v[208:211], v[78:81]
	v_mfma_f32_16x16x32_bf16 v[126:129], v[156:159], v[188:191], v[126:129]
	v_mfma_f32_16x16x32_bf16 v[122:125], v[164:167], v[188:191], v[122:125]
	v_mfma_f32_16x16x32_bf16 v[118:121], v[156:159], v[196:199], v[118:121]
	v_mfma_f32_16x16x32_bf16 v[110:113], v[164:167], v[196:199], v[110:113]
	v_mfma_f32_16x16x32_bf16 v[102:105], v[156:159], v[204:207], v[102:105]
	v_mfma_f32_16x16x32_bf16 v[94:97], v[164:167], v[204:207], v[94:97]
	v_mfma_f32_16x16x32_bf16 v[86:89], v[156:159], v[212:215], v[86:89]
	v_mfma_f32_16x16x32_bf16 v[78:81], v[164:167], v[212:215], v[78:81]
	s_setprio 0
	s_setprio 1
	v_mfma_f32_16x16x32_bf16 v[114:117], v[168:171], v[184:187], v[114:117]
	v_mfma_f32_16x16x32_bf16 v[106:109], v[176:179], v[184:187], v[106:109]
	v_mfma_f32_16x16x32_bf16 v[98:101], v[168:171], v[192:195], v[98:101]
	v_mfma_f32_16x16x32_bf16 v[90:93], v[176:179], v[192:195], v[90:93]
	v_mfma_f32_16x16x32_bf16 v[82:85], v[168:171], v[200:203], v[82:85]
	v_mfma_f32_16x16x32_bf16 v[74:77], v[176:179], v[200:203], v[74:77]
	v_mfma_f32_16x16x32_bf16 v[70:73], v[168:171], v[208:211], v[70:73]
	v_mfma_f32_16x16x32_bf16 v[66:69], v[176:179], v[208:211], v[66:69]
	v_mfma_f32_16x16x32_bf16 v[114:117], v[172:175], v[188:191], v[114:117]
	v_mfma_f32_16x16x32_bf16 v[106:109], v[180:183], v[188:191], v[106:109]
	v_mfma_f32_16x16x32_bf16 v[98:101], v[172:175], v[196:199], v[98:101]
	v_mfma_f32_16x16x32_bf16 v[90:93], v[180:183], v[196:199], v[90:93]
	v_mfma_f32_16x16x32_bf16 v[82:85], v[172:175], v[204:207], v[82:85]
	v_mfma_f32_16x16x32_bf16 v[74:77], v[180:183], v[204:207], v[74:77]
	v_mfma_f32_16x16x32_bf16 v[70:73], v[172:175], v[212:215], v[70:73]
	v_mfma_f32_16x16x32_bf16 v[66:69], v[180:183], v[212:215], v[66:69]
	s_setprio 0
	s_barrier
	s_add_i32 s26, s70, s33
	v_lshl_add_u64 v[216:217], v[216:217], 0, s[8:9]
	s_mov_b32 m0, s26
	ds_read_b128 v[184:187], v154 offset:49152
	ds_read_b128 v[188:191], v154 offset:50176
	ds_read_b128 v[192:195], v154 offset:51200
	ds_read_b128 v[196:199], v154 offset:52224
	ds_read_b128 v[200:203], v154 offset:53248
	ds_read_b128 v[204:207], v154 offset:54272
	ds_read_b128 v[208:211], v154 offset:55296
	ds_read_b128 v[212:215], v154 offset:56320
	global_load_lds_dwordx4 v[216:217], off
	s_add_i32 m0, s26, 0x2000
	s_add_u32 s24, s24, 0x80080
	v_lshl_add_u64 v[216:217], v[218:219], 0, s[8:9]
	s_addc_u32 s25, s25, 0
	s_add_i32 s26, s71, s33
	global_load_lds_dwordx4 v[216:217], off
	s_mov_b32 m0, s26
	s_nop 0
	global_load_lds_dwordx4 v134, s[24:25]
	s_add_i32 m0, s26, 0x2000
	s_nop 0
	global_load_lds_dwordx4 v130, s[24:25]
	v_lshl_add_u64 v[216:217], v[220:221], 0, s[8:9]
	s_mov_b32 m0, s44
	s_nop 0
	global_load_lds_dwordx4 v[216:217], off
	v_lshl_add_u64 v[216:217], v[222:223], 0, s[8:9]
	s_mov_b32 m0, s45
	s_nop 0
	global_load_lds_dwordx4 v[216:217], off
	s_waitcnt vmcnt(8)
	s_waitcnt lgkmcnt(0)
	s_barrier
	s_setprio 1
	s_waitcnt lgkmcnt(0)
	v_mfma_f32_16x16x32_bf16 v[62:65], v[146:149], v[184:187], v[62:65]
	v_mfma_f32_16x16x32_bf16 v[58:61], v[160:163], v[184:187], v[58:61]
	v_mfma_f32_16x16x32_bf16 v[54:57], v[146:149], v[192:195], v[54:57]
	v_mfma_f32_16x16x32_bf16 v[46:49], v[160:163], v[192:195], v[46:49]
	v_mfma_f32_16x16x32_bf16 v[38:41], v[146:149], v[200:203], v[38:41]
	v_mfma_f32_16x16x32_bf16 v[30:33], v[160:163], v[200:203], v[30:33]
	v_mfma_f32_16x16x32_bf16 v[22:25], v[146:149], v[208:211], v[22:25]
	v_mfma_f32_16x16x32_bf16 v[14:17], v[160:163], v[208:211], v[14:17]
	v_mfma_f32_16x16x32_bf16 v[62:65], v[156:159], v[188:191], v[62:65]
	v_mfma_f32_16x16x32_bf16 v[58:61], v[164:167], v[188:191], v[58:61]
	v_mfma_f32_16x16x32_bf16 v[54:57], v[156:159], v[196:199], v[54:57]
	v_mfma_f32_16x16x32_bf16 v[46:49], v[164:167], v[196:199], v[46:49]
	v_mfma_f32_16x16x32_bf16 v[38:41], v[156:159], v[204:207], v[38:41]
	v_mfma_f32_16x16x32_bf16 v[30:33], v[164:167], v[204:207], v[30:33]
	v_mfma_f32_16x16x32_bf16 v[22:25], v[156:159], v[212:215], v[22:25]
	v_mfma_f32_16x16x32_bf16 v[14:17], v[164:167], v[212:215], v[14:17]
	s_setprio 0
	s_setprio 1
	v_mfma_f32_16x16x32_bf16 v[50:53], v[168:171], v[184:187], v[50:53]
	v_mfma_f32_16x16x32_bf16 v[42:45], v[176:179], v[184:187], v[42:45]
	v_mfma_f32_16x16x32_bf16 v[34:37], v[168:171], v[192:195], v[34:37]
	v_mfma_f32_16x16x32_bf16 v[26:29], v[176:179], v[192:195], v[26:29]
	v_mfma_f32_16x16x32_bf16 v[18:21], v[168:171], v[200:203], v[18:21]
	v_mfma_f32_16x16x32_bf16 v[10:13], v[176:179], v[200:203], v[10:13]
	v_mfma_f32_16x16x32_bf16 v[6:9], v[168:171], v[208:211], v[6:9]
	v_mfma_f32_16x16x32_bf16 v[2:5], v[176:179], v[208:211], v[2:5]
	v_mfma_f32_16x16x32_bf16 v[50:53], v[172:175], v[188:191], v[50:53]
	v_mfma_f32_16x16x32_bf16 v[42:45], v[180:183], v[188:191], v[42:45]
	v_mfma_f32_16x16x32_bf16 v[34:37], v[172:175], v[196:199], v[34:37]
	v_mfma_f32_16x16x32_bf16 v[26:29], v[180:183], v[196:199], v[26:29]
	v_mfma_f32_16x16x32_bf16 v[18:21], v[172:175], v[204:207], v[18:21]
	v_mfma_f32_16x16x32_bf16 v[10:13], v[180:183], v[204:207], v[10:13]
	v_mfma_f32_16x16x32_bf16 v[6:9], v[172:175], v[212:215], v[6:9]
	v_mfma_f32_16x16x32_bf16 v[2:5], v[180:183], v[212:215], v[2:5]
	s_setprio 0
	s_barrier
	s_add_i32 s69, s69, 2
	s_add_u32 s22, s22, 0x100
	s_addc_u32 s23, s23, 0
	s_add_u32 s67, s67, 0x100
	s_addc_u32 s68, s68, 0
	s_cmp_gt_u32 s69, 29
	s_cbranch_scc0 .LBB0_767
	s_and_b64 vcc, exec, s[10:11]
	s_cbranch_vccz .LBB0_770
	s_barrier

.LBB0_1043:
	ds_read_b128 v[26:29], v209
	ds_read_b128 v[30:33], v209 offset:1024
	ds_read_b128 v[18:21], v209 offset:2048
	ds_read_b128 v[22:25], v209 offset:3072
	ds_read_b128 v[10:13], v210
	ds_read_b128 v[14:17], v210 offset:1024
	ds_read_b128 v[2:5], v210 offset:2048
	ds_read_b128 v[6:9], v210 offset:3072
	s_add_u32 s44, s40, 0xfffc0080
	s_addc_u32 s45, s41, -1
	s_cmp_eq_u32 s81, 12
	s_cselect_b32 s49, s1, s45
	s_cselect_b32 s48, s35, s44
	s_cselect_b32 s45, s31, s61
	s_cselect_b32 s44, s43, s60
	s_add_i32 m0, s65, 0xc000
	ds_read_b128 v[182:185], v211
	ds_read_b128 v[186:189], v211 offset:1024
	ds_read_b128 v[190:193], v211 offset:2048
	ds_read_b128 v[194:197], v211 offset:3072
	ds_read_b128 v[218:221], v211 offset:4096
	ds_read_b128 v[222:225], v211 offset:5120
	ds_read_b128 v[226:229], v211 offset:6144
	ds_read_b128 v[230:233], v211 offset:7168
	global_load_lds_dwordx4 v174, s[40:41]
	s_add_i32 m0, s65, 0xe000
	s_nop 0
	global_load_lds_dwordx4 v176, s[40:41]
	s_waitcnt vmcnt(8)
	s_waitcnt lgkmcnt(0)
	s_barrier
	s_setprio 1
	s_waitcnt lgkmcnt(0)
	v_mfma_scale_f32_16x16x128_f8f6f4 v[158:161], v[26:33], v[182:189], v[158:161], v212, v213 op_sel_hi:[0,0,0]
	v_mfma_scale_f32_16x16x128_f8f6f4 v[154:157], v[18:25], v[182:189], v[154:157], v212, v213 op_sel_hi:[0,0,0]
	v_mfma_scale_f32_16x16x128_f8f6f4 v[142:145], v[26:33], v[190:197], v[142:145], v212, v213 op_sel_hi:[0,0,0]
	v_mfma_scale_f32_16x16x128_f8f6f4 v[138:141], v[18:25], v[190:197], v[138:141], v212, v213 op_sel_hi:[0,0,0]
	v_mfma_scale_f32_16x16x128_f8f6f4 v[126:129], v[26:33], v[218:225], v[126:129], v212, v213 op_sel_hi:[0,0,0]
	v_mfma_scale_f32_16x16x128_f8f6f4 v[122:125], v[18:25], v[218:225], v[122:125], v212, v213 op_sel_hi:[0,0,0]
	v_mfma_scale_f32_16x16x128_f8f6f4 v[110:113], v[26:33], v[226:233], v[110:113], v212, v213 op_sel_hi:[0,0,0]
	v_mfma_scale_f32_16x16x128_f8f6f4 v[106:109], v[18:25], v[226:233], v[106:109], v212, v213 op_sel_hi:[0,0,0]
	s_setprio 0
	s_setprio 1
	v_mfma_scale_f32_16x16x128_f8f6f4 v[150:153], v[10:17], v[182:189], v[150:153], v212, v213 op_sel_hi:[0,0,0]
	v_mfma_scale_f32_16x16x128_f8f6f4 v[146:149], v[2:9], v[182:189], v[146:149], v212, v213 op_sel_hi:[0,0,0]
	v_mfma_scale_f32_16x16x128_f8f6f4 v[134:137], v[10:17], v[190:197], v[134:137], v212, v213 op_sel_hi:[0,0,0]
	v_mfma_scale_f32_16x16x128_f8f6f4 v[130:133], v[2:9], v[190:197], v[130:133], v212, v213 op_sel_hi:[0,0,0]
	v_mfma_scale_f32_16x16x128_f8f6f4 v[118:121], v[10:17], v[218:225], v[118:121], v212, v213 op_sel_hi:[0,0,0]
	v_mfma_scale_f32_16x16x128_f8f6f4 v[114:117], v[2:9], v[218:225], v[114:117], v212, v213 op_sel_hi:[0,0,0]
	v_mfma_scale_f32_16x16x128_f8f6f4 v[102:105], v[10:17], v[226:233], v[102:105], v212, v213 op_sel_hi:[0,0,0]
	v_mfma_scale_f32_16x16x128_f8f6f4 v[98:101], v[2:9], v[226:233], v[98:101], v212, v213 op_sel_hi:[0,0,0]
	s_setprio 0
	s_barrier
	s_add_i32 s82, s77, s64
	v_lshl_add_u64 v[182:183], s[44:45], 0, v[164:165]
	s_mov_b32 m0, s82
	ds_read_b128 v[190:193], v211 offset:16384
	ds_read_b128 v[194:197], v211 offset:17408
	ds_read_b128 v[218:221], v211 offset:18432
	ds_read_b128 v[222:225], v211 offset:19456
	ds_read_b128 v[226:229], v211 offset:20480
	ds_read_b128 v[230:233], v211 offset:21504
	ds_read_b128 v[234:237], v211 offset:22528
	ds_read_b128 v[238:241], v211 offset:23552
	global_load_lds_dwordx4 v164, s[44:45]
	s_add_i32 m0, s82, 0x2000
	s_add_u32 s82, s44, 0x40000
	v_lshl_add_u64 v[184:185], s[44:45], 0, v[168:169]
	s_addc_u32 s83, s45, 0
	s_add_i32 s84, s78, s64
	global_load_lds_dwordx4 v168, s[44:45]
	s_mov_b32 m0, s84
	v_lshl_add_u64 v[188:189], s[48:49], 0, v[166:167]
	global_load_lds_dwordx4 v164, s[82:83]
	s_add_i32 m0, s84, 0x2000
	s_nop 0
	global_load_lds_dwordx4 v168, s[82:83]
	v_lshl_add_u64 v[186:187], s[48:49], 0, v[162:163]
	s_mov_b32 m0, s65
	s_nop 0
	global_load_lds_dwordx4 v162, s[48:49]
	s_mov_b32 m0, s66
	s_nop 0
	global_load_lds_dwordx4 v166, s[48:49]
	s_waitcnt vmcnt(8)
	s_waitcnt lgkmcnt(0)
	s_barrier
	s_setprio 1
	s_waitcnt lgkmcnt(0)
	v_mfma_scale_f32_16x16x128_f8f6f4 v[94:97], v[26:33], v[190:197], v[94:97], v212, v213 op_sel_hi:[0,0,0]
	v_mfma_scale_f32_16x16x128_f8f6f4 v[90:93], v[18:25], v[190:197], v[90:93], v212, v213 op_sel_hi:[0,0,0]
	v_mfma_scale_f32_16x16x128_f8f6f4 v[78:81], v[26:33], v[218:225], v[78:81], v212, v213 op_sel_hi:[0,0,0]
	v_mfma_scale_f32_16x16x128_f8f6f4 v[74:77], v[18:25], v[218:225], v[74:77], v212, v213 op_sel_hi:[0,0,0]
	v_mfma_scale_f32_16x16x128_f8f6f4 v[62:65], v[26:33], v[226:233], v[62:65], v212, v213 op_sel_hi:[0,0,0]
	v_mfma_scale_f32_16x16x128_f8f6f4 v[58:61], v[18:25], v[226:233], v[58:61], v212, v213 op_sel_hi:[0,0,0]
	v_mfma_scale_f32_16x16x128_f8f6f4 v[46:49], v[26:33], v[234:241], v[46:49], v212, v213 op_sel_hi:[0,0,0]
	v_mfma_scale_f32_16x16x128_f8f6f4 v[42:45], v[18:25], v[234:241], v[42:45], v212, v213 op_sel_hi:[0,0,0]
	s_setprio 0
	s_setprio 1
	v_mfma_scale_f32_16x16x128_f8f6f4 v[86:89], v[10:17], v[190:197], v[86:89], v212, v213 op_sel_hi:[0,0,0]
	v_mfma_scale_f32_16x16x128_f8f6f4 v[82:85], v[2:9], v[190:197], v[82:85], v212, v213 op_sel_hi:[0,0,0]
	v_mfma_scale_f32_16x16x128_f8f6f4 v[70:73], v[10:17], v[218:225], v[70:73], v212, v213 op_sel_hi:[0,0,0]
	v_mfma_scale_f32_16x16x128_f8f6f4 v[66:69], v[2:9], v[218:225], v[66:69], v212, v213 op_sel_hi:[0,0,0]
	v_mfma_scale_f32_16x16x128_f8f6f4 v[54:57], v[10:17], v[226:233], v[54:57], v212, v213 op_sel_hi:[0,0,0]
	v_mfma_scale_f32_16x16x128_f8f6f4 v[50:53], v[2:9], v[226:233], v[50:53], v212, v213 op_sel_hi:[0,0,0]
	v_mfma_scale_f32_16x16x128_f8f6f4 v[38:41], v[10:17], v[234:241], v[38:41], v212, v213 op_sel_hi:[0,0,0]
	v_mfma_scale_f32_16x16x128_f8f6f4 v[34:37], v[2:9], v[234:241], v[34:37], v212, v213 op_sel_hi:[0,0,0]
	s_setprio 0
	s_barrier
	s_add_i32 s82, 0, 0x18000
	s_add_i32 s83, 0, 0x1c000
	v_add_u32_e32 v14, s82, v202
	v_add_u32_e32 v30, s83, v202
	ds_read_b128 v[2:5], v14
	ds_read_b128 v[6:9], v14 offset:1024
	ds_read_b128 v[10:13], v14 offset:2048
	ds_read_b128 v[14:17], v14 offset:3072
	ds_read_b128 v[18:21], v30
	ds_read_b128 v[22:25], v30 offset:1024
	ds_read_b128 v[26:29], v30 offset:2048
	ds_read_b128 v[30:33], v30 offset:3072
	s_add_u32 s48, s48, 0x40000
	s_addc_u32 s49, s49, 0
	s_mov_b32 m0, s67
	ds_read_b128 v[190:193], v211 offset:32768
	ds_read_b128 v[194:197], v211 offset:33792
	ds_read_b128 v[218:221], v211 offset:34816
	ds_read_b128 v[222:225], v211 offset:35840
	ds_read_b128 v[226:229], v211 offset:36864
	ds_read_b128 v[230:233], v211 offset:37888
	ds_read_b128 v[234:237], v211 offset:38912
	ds_read_b128 v[238:241], v211 offset:39936
	global_load_lds_dwordx4 v162, s[48:49]
	s_mov_b32 m0, s68
	s_nop 0
	global_load_lds_dwordx4 v166, s[48:49]
	s_waitcnt vmcnt(8)
	s_waitcnt lgkmcnt(0)
	s_barrier
	s_setprio 1
	s_waitcnt lgkmcnt(0)
	v_mfma_scale_f32_16x16x128_f8f6f4 v[158:161], v[2:9], v[190:197], v[158:161], v212, v213 op_sel_hi:[0,0,0]
	v_mfma_scale_f32_16x16x128_f8f6f4 v[154:157], v[10:17], v[190:197], v[154:157], v212, v213 op_sel_hi:[0,0,0]
	v_mfma_scale_f32_16x16x128_f8f6f4 v[142:145], v[2:9], v[218:225], v[142:145], v212, v213 op_sel_hi:[0,0,0]
	v_mfma_scale_f32_16x16x128_f8f6f4 v[138:141], v[10:17], v[218:225], v[138:141], v212, v213 op_sel_hi:[0,0,0]
	v_mfma_scale_f32_16x16x128_f8f6f4 v[126:129], v[2:9], v[226:233], v[126:129], v212, v213 op_sel_hi:[0,0,0]
	v_mfma_scale_f32_16x16x128_f8f6f4 v[122:125], v[10:17], v[226:233], v[122:125], v212, v213 op_sel_hi:[0,0,0]
	v_mfma_scale_f32_16x16x128_f8f6f4 v[110:113], v[2:9], v[234:241], v[110:113], v212, v213 op_sel_hi:[0,0,0]
	v_mfma_scale_f32_16x16x128_f8f6f4 v[106:109], v[10:17], v[234:241], v[106:109], v212, v213 op_sel_hi:[0,0,0]
	s_setprio 0
	s_setprio 1
	v_mfma_scale_f32_16x16x128_f8f6f4 v[150:153], v[18:25], v[190:197], v[150:153], v212, v213 op_sel_hi:[0,0,0]
	v_mfma_scale_f32_16x16x128_f8f6f4 v[146:149], v[26:33], v[190:197], v[146:149], v212, v213 op_sel_hi:[0,0,0]
	v_mfma_scale_f32_16x16x128_f8f6f4 v[134:137], v[18:25], v[218:225], v[134:137], v212, v213 op_sel_hi:[0,0,0]
	v_mfma_scale_f32_16x16x128_f8f6f4 v[130:133], v[26:33], v[218:225], v[130:133], v212, v213 op_sel_hi:[0,0,0]
	v_mfma_scale_f32_16x16x128_f8f6f4 v[118:121], v[18:25], v[226:233], v[118:121], v212, v213 op_sel_hi:[0,0,0]
	v_mfma_scale_f32_16x16x128_f8f6f4 v[114:117], v[26:33], v[226:233], v[114:117], v212, v213 op_sel_hi:[0,0,0]
	v_mfma_scale_f32_16x16x128_f8f6f4 v[102:105], v[18:25], v[234:241], v[102:105], v212, v213 op_sel_hi:[0,0,0]
	v_mfma_scale_f32_16x16x128_f8f6f4 v[98:101], v[26:33], v[234:241], v[98:101], v212, v213 op_sel_hi:[0,0,0]
	s_setprio 0
	s_barrier
	s_add_i32 s48, s82, s64
	v_lshl_add_u64 v[182:183], v[182:183], 0, s[24:25]
	s_mov_b32 m0, s48
	ds_read_b128 v[190:193], v211 offset:49152
	ds_read_b128 v[194:197], v211 offset:50176
	ds_read_b128 v[218:221], v211 offset:51200
	ds_read_b128 v[222:225], v211 offset:52224
	ds_read_b128 v[226:229], v211 offset:53248
	ds_read_b128 v[230:233], v211 offset:54272
	ds_read_b128 v[234:237], v211 offset:55296
	ds_read_b128 v[238:241], v211 offset:56320
	global_load_lds_dwordx4 v[182:183], off
	s_add_i32 m0, s48, 0x2000
	s_add_u32 s44, s44, 0x40080
	v_lshl_add_u64 v[182:183], v[184:185], 0, s[24:25]
	s_addc_u32 s45, s45, 0
	s_add_i32 s48, s83, s64
	global_load_lds_dwordx4 v[182:183], off
	s_mov_b32 m0, s48
	s_nop 0
	global_load_lds_dwordx4 v164, s[44:45]
	s_add_i32 m0, s48, 0x2000
	s_nop 0
	global_load_lds_dwordx4 v168, s[44:45]
	v_lshl_add_u64 v[182:183], v[186:187], 0, s[24:25]
	s_mov_b32 m0, s72
	s_nop 0
	global_load_lds_dwordx4 v[182:183], off
	v_lshl_add_u64 v[182:183], v[188:189], 0, s[24:25]
	s_mov_b32 m0, s73
	s_nop 0
	global_load_lds_dwordx4 v[182:183], off
	s_waitcnt vmcnt(8)
	s_waitcnt lgkmcnt(0)
	s_barrier
	s_setprio 1
	s_waitcnt lgkmcnt(0)
	v_mfma_scale_f32_16x16x128_f8f6f4 v[94:97], v[2:9], v[190:197], v[94:97], v212, v213 op_sel_hi:[0,0,0]
	v_mfma_scale_f32_16x16x128_f8f6f4 v[90:93], v[10:17], v[190:197], v[90:93], v212, v213 op_sel_hi:[0,0,0]
	v_mfma_scale_f32_16x16x128_f8f6f4 v[78:81], v[2:9], v[218:225], v[78:81], v212, v213 op_sel_hi:[0,0,0]
	v_mfma_scale_f32_16x16x128_f8f6f4 v[74:77], v[10:17], v[218:225], v[74:77], v212, v213 op_sel_hi:[0,0,0]
	v_mfma_scale_f32_16x16x128_f8f6f4 v[62:65], v[2:9], v[226:233], v[62:65], v212, v213 op_sel_hi:[0,0,0]
	v_mfma_scale_f32_16x16x128_f8f6f4 v[58:61], v[10:17], v[226:233], v[58:61], v212, v213 op_sel_hi:[0,0,0]
	v_mfma_scale_f32_16x16x128_f8f6f4 v[46:49], v[2:9], v[234:241], v[46:49], v212, v213 op_sel_hi:[0,0,0]
	v_mfma_scale_f32_16x16x128_f8f6f4 v[42:45], v[10:17], v[234:241], v[42:45], v212, v213 op_sel_hi:[0,0,0]
	s_setprio 0
	s_setprio 1
	v_mfma_scale_f32_16x16x128_f8f6f4 v[86:89], v[18:25], v[190:197], v[86:89], v212, v213 op_sel_hi:[0,0,0]
	v_mfma_scale_f32_16x16x128_f8f6f4 v[82:85], v[26:33], v[190:197], v[82:85], v212, v213 op_sel_hi:[0,0,0]
	v_mfma_scale_f32_16x16x128_f8f6f4 v[70:73], v[18:25], v[218:225], v[70:73], v212, v213 op_sel_hi:[0,0,0]
	v_mfma_scale_f32_16x16x128_f8f6f4 v[66:69], v[26:33], v[218:225], v[66:69], v212, v213 op_sel_hi:[0,0,0]
	v_mfma_scale_f32_16x16x128_f8f6f4 v[54:57], v[18:25], v[226:233], v[54:57], v212, v213 op_sel_hi:[0,0,0]
	v_mfma_scale_f32_16x16x128_f8f6f4 v[50:53], v[26:33], v[226:233], v[50:53], v212, v213 op_sel_hi:[0,0,0]
	v_mfma_scale_f32_16x16x128_f8f6f4 v[38:41], v[18:25], v[234:241], v[38:41], v212, v213 op_sel_hi:[0,0,0]
	v_mfma_scale_f32_16x16x128_f8f6f4 v[34:37], v[26:33], v[234:241], v[34:37], v212, v213 op_sel_hi:[0,0,0]
	s_setprio 0
	s_barrier
	s_add_i32 s81, s81, 2
	s_add_u32 s40, s40, 0x100
	s_addc_u32 s41, s41, 0
	s_add_u32 s60, s60, 0x100
	s_addc_u32 s61, s61, 0
	s_cmp_gt_u32 s81, 13
	s_cbranch_scc0 .LBB0_1043
	s_and_b64 vcc, exec, s[26:27]
	s_cbranch_vccz .LBB0_1046
	s_barrier

.LBB0_1257:
	ds_read_b128 v[20:23], v202
	ds_read_b128 v[166:169], v202 offset:1024
	ds_read_b128 v[14:17], v202 offset:2048
	ds_read_b128 v[162:165], v202 offset:3072
	ds_read_b128 v[8:11], v203
	ds_read_b128 v[158:161], v203 offset:1024
	ds_read_b128 v[2:5], v203 offset:2048
	ds_read_b128 v[154:157], v203 offset:3072
	s_add_u32 s22, s20, 0xfffc0080
	s_addc_u32 s23, s21, -1
	s_cmp_eq_u32 s63, 12
	s_cselect_b32 s25, s11, s23
	s_cselect_b32 s24, s49, s22
	s_cselect_b32 s23, s13, s62
	s_cselect_b32 s22, s60, s61
	s_add_i32 m0, s35, 0xc000
	ds_read_b128 v[184:187], v204
	ds_read_b128 v[188:191], v204 offset:1024
	ds_read_b128 v[206:209], v204 offset:2048
	ds_read_b128 v[222:225], v204 offset:3072
	ds_read_b128 v[212:215], v204 offset:4096
	ds_read_b128 v[226:229], v204 offset:5120
	ds_read_b128 v[218:221], v204 offset:6144
	ds_read_b128 v[230:233], v204 offset:7168
	global_load_lds_dwordx4 v180, s[20:21]
	s_add_i32 m0, s35, 0xe000
	s_nop 0
	global_load_lds_dwordx4 v182, s[20:21]
	s_waitcnt vmcnt(8)
	s_waitcnt lgkmcnt(0)
	s_barrier
	s_setprio 1
	s_waitcnt lgkmcnt(0)
	v_mov_b32_e32 v24, v166
	v_mov_b32_e32 v25, v167
	s_nop 1
	v_mfma_scale_f32_16x16x128_f8f6f4 v[150:153], v[20:25], v[184:189], v[150:153], v168, v190 op_sel_hi:[0,0,0] cbsz:2 blgp:2
	v_mov_b32_e32 v18, v162
	v_mov_b32_e32 v19, v163
	s_nop 1
	v_mfma_scale_f32_16x16x128_f8f6f4 v[138:141], v[14:19], v[184:189], v[138:141], v164, v190 op_sel_hi:[0,0,0] cbsz:2 blgp:2
	v_mov_b32_e32 v210, v222
	v_mov_b32_e32 v211, v223
	s_nop 1
	v_mfma_scale_f32_16x16x128_f8f6f4 v[134:137], v[20:25], v[206:211], v[134:137], v168, v224 op_sel_hi:[0,0,0] cbsz:2 blgp:2
	s_nop 1
	v_mfma_scale_f32_16x16x128_f8f6f4 v[122:125], v[14:19], v[206:211], v[122:125], v164, v224 op_sel_hi:[0,0,0] cbsz:2 blgp:2
	v_mov_b32_e32 v216, v226
	v_mov_b32_e32 v217, v227
	s_nop 1
	v_mfma_scale_f32_16x16x128_f8f6f4 v[118:121], v[20:25], v[212:217], v[118:121], v168, v228 op_sel_hi:[0,0,0] cbsz:2 blgp:2
	s_nop 1
	v_mfma_scale_f32_16x16x128_f8f6f4 v[106:109], v[14:19], v[212:217], v[106:109], v164, v228 op_sel_hi:[0,0,0] cbsz:2 blgp:2
	v_mov_b32_e32 v222, v230
	v_mov_b32_e32 v223, v231
	s_nop 1
	v_mfma_scale_f32_16x16x128_f8f6f4 v[102:105], v[20:25], v[218:223], v[102:105], v168, v232 op_sel_hi:[0,0,0] cbsz:2 blgp:2
	s_nop 1
	v_mfma_scale_f32_16x16x128_f8f6f4 v[90:93], v[14:19], v[218:223], v[90:93], v164, v232 op_sel_hi:[0,0,0] cbsz:2 blgp:2
	s_setprio 0
	s_setprio 1
	v_mov_b32_e32 v12, v158
	v_mov_b32_e32 v13, v159
	s_nop 1
	v_mfma_scale_f32_16x16x128_f8f6f4 v[146:149], v[8:13], v[184:189], v[146:149], v160, v190 op_sel_hi:[0,0,0] cbsz:2 blgp:2
	v_mov_b32_e32 v6, v154
	v_mov_b32_e32 v7, v155
	s_nop 1
	v_mfma_scale_f32_16x16x128_f8f6f4 v[142:145], v[2:7], v[184:189], v[142:145], v156, v190 op_sel_hi:[0,0,0] cbsz:2 blgp:2
	s_nop 1
	v_mfma_scale_f32_16x16x128_f8f6f4 v[130:133], v[8:13], v[206:211], v[130:133], v160, v224 op_sel_hi:[0,0,0] cbsz:2 blgp:2
	s_nop 1
	v_mfma_scale_f32_16x16x128_f8f6f4 v[126:129], v[2:7], v[206:211], v[126:129], v156, v224 op_sel_hi:[0,0,0] cbsz:2 blgp:2
	s_nop 1
	v_mfma_scale_f32_16x16x128_f8f6f4 v[114:117], v[8:13], v[212:217], v[114:117], v160, v228 op_sel_hi:[0,0,0] cbsz:2 blgp:2
	s_nop 1
	v_mfma_scale_f32_16x16x128_f8f6f4 v[110:113], v[2:7], v[212:217], v[110:113], v156, v228 op_sel_hi:[0,0,0] cbsz:2 blgp:2
	s_nop 1
	v_mfma_scale_f32_16x16x128_f8f6f4 v[98:101], v[8:13], v[218:223], v[98:101], v160, v232 op_sel_hi:[0,0,0] cbsz:2 blgp:2
	s_nop 1
	v_mfma_scale_f32_16x16x128_f8f6f4 v[94:97], v[2:7], v[218:223], v[94:97], v156, v232 op_sel_hi:[0,0,0] cbsz:2 blgp:2
	s_setprio 0
	s_barrier
	s_add_i32 s64, s42, s27
	v_lshl_add_u64 v[184:185], s[22:23], 0, v[172:173]
	s_mov_b32 m0, s64
	ds_read_b128 v[206:209], v204 offset:16384
	ds_read_b128 v[228:231], v204 offset:17408
	ds_read_b128 v[212:215], v204 offset:18432
	ds_read_b128 v[232:235], v204 offset:19456
	ds_read_b128 v[218:221], v204 offset:20480
	ds_read_b128 v[236:239], v204 offset:21504
	ds_read_b128 v[224:227], v204 offset:22528
	ds_read_b128 v[240:243], v204 offset:23552
	global_load_lds_dwordx4 v172, s[22:23]
	s_add_i32 m0, s64, 0x2000
	s_add_u32 s64, s22, 0x40000
	v_lshl_add_u64 v[186:187], s[22:23], 0, v[174:175]
	s_addc_u32 s65, s23, 0
	s_add_i32 s66, s43, s27
	global_load_lds_dwordx4 v174, s[22:23]
	s_mov_b32 m0, s66
	v_lshl_add_u64 v[188:189], s[24:25], 0, v[178:179]
	global_load_lds_dwordx4 v172, s[64:65]
	s_add_i32 m0, s66, 0x2000
	v_lshl_add_u64 v[190:191], s[24:25], 0, v[176:177]
	global_load_lds_dwordx4 v174, s[64:65]
	s_mov_b32 m0, s35
	s_nop 0
	global_load_lds_dwordx4 v178, s[24:25]
	s_mov_b32 m0, s36
	s_nop 0
	global_load_lds_dwordx4 v176, s[24:25]
	s_waitcnt vmcnt(8)
	s_waitcnt lgkmcnt(0)
	s_barrier
	s_setprio 1
	s_waitcnt lgkmcnt(0)
	v_mov_b32_e32 v210, v228
	v_mov_b32_e32 v211, v229
	s_nop 1
	v_mfma_scale_f32_16x16x128_f8f6f4 v[86:89], v[20:25], v[206:211], v[86:89], v168, v230 op_sel_hi:[0,0,0] cbsz:2 blgp:2
	s_nop 1
	v_mfma_scale_f32_16x16x128_f8f6f4 v[74:77], v[14:19], v[206:211], v[74:77], v164, v230 op_sel_hi:[0,0,0] cbsz:2 blgp:2
	v_mov_b32_e32 v216, v232
	v_mov_b32_e32 v217, v233
	s_nop 1
	v_mfma_scale_f32_16x16x128_f8f6f4 v[70:73], v[20:25], v[212:217], v[70:73], v168, v234 op_sel_hi:[0,0,0] cbsz:2 blgp:2
	s_nop 1
	v_mfma_scale_f32_16x16x128_f8f6f4 v[58:61], v[14:19], v[212:217], v[58:61], v164, v234 op_sel_hi:[0,0,0] cbsz:2 blgp:2
	v_mov_b32_e32 v222, v236
	v_mov_b32_e32 v223, v237
	s_nop 1
	v_mfma_scale_f32_16x16x128_f8f6f4 v[54:57], v[20:25], v[218:223], v[54:57], v168, v238 op_sel_hi:[0,0,0] cbsz:2 blgp:2
	s_nop 1
	v_mfma_scale_f32_16x16x128_f8f6f4 v[42:45], v[14:19], v[218:223], v[42:45], v164, v238 op_sel_hi:[0,0,0] cbsz:2 blgp:2
	v_mov_b32_e32 v228, v240
	v_mov_b32_e32 v229, v241
	s_nop 1
	v_mfma_scale_f32_16x16x128_f8f6f4 v[38:41], v[20:25], v[224:229], v[38:41], v168, v242 op_sel_hi:[0,0,0] cbsz:2 blgp:2
	s_nop 1
	v_mfma_scale_f32_16x16x128_f8f6f4 v[26:29], v[14:19], v[224:229], v[26:29], v164, v242 op_sel_hi:[0,0,0] cbsz:2 blgp:2
	s_setprio 0
	s_setprio 1
	s_nop 1
	v_mfma_scale_f32_16x16x128_f8f6f4 v[82:85], v[8:13], v[206:211], v[82:85], v160, v230 op_sel_hi:[0,0,0] cbsz:2 blgp:2
	s_nop 1
	v_mfma_scale_f32_16x16x128_f8f6f4 v[78:81], v[2:7], v[206:211], v[78:81], v156, v230 op_sel_hi:[0,0,0] cbsz:2 blgp:2
	s_nop 1
	v_mfma_scale_f32_16x16x128_f8f6f4 v[66:69], v[8:13], v[212:217], v[66:69], v160, v234 op_sel_hi:[0,0,0] cbsz:2 blgp:2
	s_nop 1
	v_mfma_scale_f32_16x16x128_f8f6f4 v[62:65], v[2:7], v[212:217], v[62:65], v156, v234 op_sel_hi:[0,0,0] cbsz:2 blgp:2
	s_nop 1
	v_mfma_scale_f32_16x16x128_f8f6f4 v[50:53], v[8:13], v[218:223], v[50:53], v160, v238 op_sel_hi:[0,0,0] cbsz:2 blgp:2
	s_nop 1
	v_mfma_scale_f32_16x16x128_f8f6f4 v[46:49], v[2:7], v[218:223], v[46:49], v156, v238 op_sel_hi:[0,0,0] cbsz:2 blgp:2
	s_nop 1
	v_mfma_scale_f32_16x16x128_f8f6f4 v[34:37], v[8:13], v[224:229], v[34:37], v160, v242 op_sel_hi:[0,0,0] cbsz:2 blgp:2
	s_nop 1
	v_mfma_scale_f32_16x16x128_f8f6f4 v[30:33], v[2:7], v[224:229], v[30:33], v156, v242 op_sel_hi:[0,0,0] cbsz:2 blgp:2
	s_setprio 0
	s_barrier
	s_add_i32 s64, 0, 0x18000
	s_add_i32 s65, 0, 0x1c000
	v_add_u32_e32 v2, s64, v198
	v_add_u32_e32 v6, s65, v198
	ds_read_b128 v[20:23], v2
	ds_read_b128 v[166:169], v2 offset:1024
	ds_read_b128 v[14:17], v2 offset:2048
	ds_read_b128 v[162:165], v2 offset:3072
	ds_read_b128 v[8:11], v6
	ds_read_b128 v[154:157], v6 offset:1024
	ds_read_b128 v[2:5], v6 offset:2048
	ds_read_b128 v[158:161], v6 offset:3072
	s_add_u32 s24, s24, 0x40000
	s_addc_u32 s25, s25, 0
	s_mov_b32 m0, s37
	ds_read_b128 v[206:209], v204 offset:32768
	ds_read_b128 v[228:231], v204 offset:33792
	ds_read_b128 v[212:215], v204 offset:34816
	ds_read_b128 v[232:235], v204 offset:35840
	ds_read_b128 v[218:221], v204 offset:36864
	ds_read_b128 v[236:239], v204 offset:37888
	ds_read_b128 v[224:227], v204 offset:38912
	ds_read_b128 v[240:243], v204 offset:39936
	global_load_lds_dwordx4 v178, s[24:25]
	s_mov_b32 m0, s38
	s_nop 0
	global_load_lds_dwordx4 v176, s[24:25]
	s_waitcnt vmcnt(8)
	s_waitcnt lgkmcnt(0)
	s_barrier
	s_setprio 1
	s_waitcnt lgkmcnt(0)
	v_mov_b32_e32 v24, v166
	v_mov_b32_e32 v25, v167
	v_mov_b32_e32 v210, v228
	v_mov_b32_e32 v211, v229
	s_nop 1
	v_mfma_scale_f32_16x16x128_f8f6f4 v[150:153], v[20:25], v[206:211], v[150:153], v168, v230 op_sel_hi:[0,0,0] cbsz:2 blgp:2
	v_mov_b32_e32 v18, v162
	v_mov_b32_e32 v19, v163
	s_nop 1
	v_mfma_scale_f32_16x16x128_f8f6f4 v[138:141], v[14:19], v[206:211], v[138:141], v164, v230 op_sel_hi:[0,0,0] cbsz:2 blgp:2
	v_mov_b32_e32 v216, v232
	v_mov_b32_e32 v217, v233
	s_nop 1
	v_mfma_scale_f32_16x16x128_f8f6f4 v[134:137], v[20:25], v[212:217], v[134:137], v168, v234 op_sel_hi:[0,0,0] cbsz:2 blgp:2
	s_nop 1
	v_mfma_scale_f32_16x16x128_f8f6f4 v[122:125], v[14:19], v[212:217], v[122:125], v164, v234 op_sel_hi:[0,0,0] cbsz:2 blgp:2
	v_mov_b32_e32 v222, v236
	v_mov_b32_e32 v223, v237
	s_nop 1
	v_mfma_scale_f32_16x16x128_f8f6f4 v[118:121], v[20:25], v[218:223], v[118:121], v168, v238 op_sel_hi:[0,0,0] cbsz:2 blgp:2
	s_nop 1
	v_mfma_scale_f32_16x16x128_f8f6f4 v[106:109], v[14:19], v[218:223], v[106:109], v164, v238 op_sel_hi:[0,0,0] cbsz:2 blgp:2
	v_mov_b32_e32 v228, v240
	v_mov_b32_e32 v229, v241
	s_nop 1
	v_mfma_scale_f32_16x16x128_f8f6f4 v[102:105], v[20:25], v[224:229], v[102:105], v168, v242 op_sel_hi:[0,0,0] cbsz:2 blgp:2
	s_nop 1
	v_mfma_scale_f32_16x16x128_f8f6f4 v[90:93], v[14:19], v[224:229], v[90:93], v164, v242 op_sel_hi:[0,0,0] cbsz:2 blgp:2
	s_setprio 0
	s_setprio 1
	v_mov_b32_e32 v12, v154
	v_mov_b32_e32 v13, v155
	s_nop 1
	v_mfma_scale_f32_16x16x128_f8f6f4 v[146:149], v[8:13], v[206:211], v[146:149], v156, v230 op_sel_hi:[0,0,0] cbsz:2 blgp:2
	v_mov_b32_e32 v6, v158
	v_mov_b32_e32 v7, v159
	s_nop 1
	v_mfma_scale_f32_16x16x128_f8f6f4 v[142:145], v[2:7], v[206:211], v[142:145], v160, v230 op_sel_hi:[0,0,0] cbsz:2 blgp:2
	s_nop 1
	v_mfma_scale_f32_16x16x128_f8f6f4 v[130:133], v[8:13], v[212:217], v[130:133], v156, v234 op_sel_hi:[0,0,0] cbsz:2 blgp:2
	s_nop 1
	v_mfma_scale_f32_16x16x128_f8f6f4 v[126:129], v[2:7], v[212:217], v[126:129], v160, v234 op_sel_hi:[0,0,0] cbsz:2 blgp:2
	s_nop 1
	v_mfma_scale_f32_16x16x128_f8f6f4 v[114:117], v[8:13], v[218:223], v[114:117], v156, v238 op_sel_hi:[0,0,0] cbsz:2 blgp:2
	s_nop 1
	v_mfma_scale_f32_16x16x128_f8f6f4 v[110:113], v[2:7], v[218:223], v[110:113], v160, v238 op_sel_hi:[0,0,0] cbsz:2 blgp:2
	s_nop 1
	v_mfma_scale_f32_16x16x128_f8f6f4 v[98:101], v[8:13], v[224:229], v[98:101], v156, v242 op_sel_hi:[0,0,0] cbsz:2 blgp:2
	s_nop 1
	v_mfma_scale_f32_16x16x128_f8f6f4 v[94:97], v[2:7], v[224:229], v[94:97], v160, v242 op_sel_hi:[0,0,0] cbsz:2 blgp:2
	s_setprio 0
	s_barrier
	s_add_i32 s24, s64, s27
	v_lshl_add_u64 v[154:155], v[184:185], 0, s[6:7]
	s_mov_b32 m0, s24
	ds_read_b128 v[206:209], v204 offset:49152
	ds_read_b128 v[228:231], v204 offset:50176
	ds_read_b128 v[212:215], v204 offset:51200
	ds_read_b128 v[232:235], v204 offset:52224
	ds_read_b128 v[218:221], v204 offset:53248
	ds_read_b128 v[236:239], v204 offset:54272
	ds_read_b128 v[224:227], v204 offset:55296
	ds_read_b128 v[240:243], v204 offset:56320
	global_load_lds_dwordx4 v[154:155], off
	s_add_i32 m0, s24, 0x2000
	s_add_u32 s22, s22, 0x40080
	v_lshl_add_u64 v[154:155], v[186:187], 0, s[6:7]
	s_addc_u32 s23, s23, 0
	s_add_i32 s24, s65, s27
	global_load_lds_dwordx4 v[154:155], off
	s_mov_b32 m0, s24
	s_nop 0
	global_load_lds_dwordx4 v172, s[22:23]
	s_add_i32 m0, s24, 0x2000
	s_nop 0
	global_load_lds_dwordx4 v174, s[22:23]
	v_lshl_add_u64 v[154:155], v[188:189], 0, s[6:7]
	s_mov_b32 m0, s39
	s_nop 0
	global_load_lds_dwordx4 v[154:155], off
	v_lshl_add_u64 v[154:155], v[190:191], 0, s[6:7]
	s_mov_b32 m0, s40
	s_nop 0
	global_load_lds_dwordx4 v[154:155], off
	s_waitcnt vmcnt(8)
	s_waitcnt lgkmcnt(0)
	s_barrier
	s_setprio 1
	s_waitcnt lgkmcnt(0)
	v_mov_b32_e32 v210, v228
	v_mov_b32_e32 v211, v229
	s_nop 1
	v_mfma_scale_f32_16x16x128_f8f6f4 v[86:89], v[20:25], v[206:211], v[86:89], v168, v230 op_sel_hi:[0,0,0] cbsz:2 blgp:2
	s_nop 1
	v_mfma_scale_f32_16x16x128_f8f6f4 v[74:77], v[14:19], v[206:211], v[74:77], v164, v230 op_sel_hi:[0,0,0] cbsz:2 blgp:2
	v_mov_b32_e32 v216, v232
	v_mov_b32_e32 v217, v233
	s_nop 1
	v_mfma_scale_f32_16x16x128_f8f6f4 v[70:73], v[20:25], v[212:217], v[70:73], v168, v234 op_sel_hi:[0,0,0] cbsz:2 blgp:2
	s_nop 1
	v_mfma_scale_f32_16x16x128_f8f6f4 v[58:61], v[14:19], v[212:217], v[58:61], v164, v234 op_sel_hi:[0,0,0] cbsz:2 blgp:2
	v_mov_b32_e32 v222, v236
	v_mov_b32_e32 v223, v237
	s_nop 1
	v_mfma_scale_f32_16x16x128_f8f6f4 v[54:57], v[20:25], v[218:223], v[54:57], v168, v238 op_sel_hi:[0,0,0] cbsz:2 blgp:2
	s_nop 1
	v_mfma_scale_f32_16x16x128_f8f6f4 v[42:45], v[14:19], v[218:223], v[42:45], v164, v238 op_sel_hi:[0,0,0] cbsz:2 blgp:2
	v_mov_b32_e32 v228, v240
	v_mov_b32_e32 v229, v241
	s_nop 1
	v_mfma_scale_f32_16x16x128_f8f6f4 v[38:41], v[20:25], v[224:229], v[38:41], v168, v242 op_sel_hi:[0,0,0] cbsz:2 blgp:2
	s_nop 1
	v_mfma_scale_f32_16x16x128_f8f6f4 v[26:29], v[14:19], v[224:229], v[26:29], v164, v242 op_sel_hi:[0,0,0] cbsz:2 blgp:2
	s_setprio 0
	s_setprio 1
	s_nop 1
	v_mfma_scale_f32_16x16x128_f8f6f4 v[82:85], v[8:13], v[206:211], v[82:85], v156, v230 op_sel_hi:[0,0,0] cbsz:2 blgp:2
	s_nop 1
	v_mfma_scale_f32_16x16x128_f8f6f4 v[78:81], v[2:7], v[206:211], v[78:81], v160, v230 op_sel_hi:[0,0,0] cbsz:2 blgp:2
	s_nop 1
	v_mfma_scale_f32_16x16x128_f8f6f4 v[66:69], v[8:13], v[212:217], v[66:69], v156, v234 op_sel_hi:[0,0,0] cbsz:2 blgp:2
	s_nop 1
	v_mfma_scale_f32_16x16x128_f8f6f4 v[62:65], v[2:7], v[212:217], v[62:65], v160, v234 op_sel_hi:[0,0,0] cbsz:2 blgp:2
	s_nop 1
	v_mfma_scale_f32_16x16x128_f8f6f4 v[50:53], v[8:13], v[218:223], v[50:53], v156, v238 op_sel_hi:[0,0,0] cbsz:2 blgp:2
	s_nop 1
	v_mfma_scale_f32_16x16x128_f8f6f4 v[46:49], v[2:7], v[218:223], v[46:49], v160, v238 op_sel_hi:[0,0,0] cbsz:2 blgp:2
	s_nop 1
	v_mfma_scale_f32_16x16x128_f8f6f4 v[34:37], v[8:13], v[224:229], v[34:37], v156, v242 op_sel_hi:[0,0,0] cbsz:2 blgp:2
	s_nop 1
	v_mfma_scale_f32_16x16x128_f8f6f4 v[30:33], v[2:7], v[224:229], v[30:33], v160, v242 op_sel_hi:[0,0,0] cbsz:2 blgp:2
	s_setprio 0
	s_barrier
	s_add_i32 s63, s63, 2
	s_add_u32 s20, s20, 0x100
	s_addc_u32 s21, s21, 0
	s_add_u32 s61, s61, 0x100
	s_addc_u32 s62, s62, 0
	s_cmp_gt_u32 s63, 13
	s_cbranch_scc0 .LBB0_1257
	s_and_b64 vcc, exec, s[8:9]
	s_cbranch_vccz .LBB0_1260
	s_barrier

.LBB0_1279:
	ds_read_b128 v[20:23], v195
	ds_read_b128 v[166:169], v195 offset:1024
	ds_read_b128 v[14:17], v195 offset:2048
	ds_read_b128 v[162:165], v195 offset:3072
	ds_read_b128 v[8:11], v196
	ds_read_b128 v[158:161], v196 offset:1024
	ds_read_b128 v[2:5], v196 offset:2048
	ds_read_b128 v[154:157], v196 offset:3072
	s_add_u32 s24, s22, 0xfffc0080
	s_addc_u32 s25, s23, -1
	s_cmp_eq_u32 s61, 12
	s_cselect_b32 s27, s11, s25
	s_cselect_b32 s26, s49, s24
	s_cselect_b32 s25, s13, s60
	s_cselect_b32 s24, s50, s51
	s_mov_b32 m0, s46
	ds_read_b128 v[184:187], v198
	ds_read_b128 v[188:191], v198 offset:1024
	ds_read_b128 v[202:205], v198 offset:2048
	ds_read_b128 v[218:221], v198 offset:3072
	ds_read_b128 v[208:211], v198 offset:4096
	ds_read_b128 v[222:225], v198 offset:5120
	ds_read_b128 v[214:217], v198 offset:6144
	ds_read_b128 v[226:229], v198 offset:7168
	global_load_lds_dwordx4 v180, s[22:23]
	s_add_i32 m0, s21, 0xe000
	s_nop 0
	global_load_lds_dwordx4 v182, s[22:23]
	s_waitcnt vmcnt(8)
	s_waitcnt lgkmcnt(0)
	s_barrier
	s_setprio 1
	s_waitcnt lgkmcnt(0)
	v_mov_b32_e32 v24, v166
	v_mov_b32_e32 v25, v167
	s_nop 1
	v_mfma_scale_f32_16x16x128_f8f6f4 v[150:153], v[20:25], v[184:189], v[150:153], v168, v190 op_sel_hi:[0,0,0] cbsz:2 blgp:2
	v_mov_b32_e32 v18, v162
	v_mov_b32_e32 v19, v163
	s_nop 1
	v_mfma_scale_f32_16x16x128_f8f6f4 v[138:141], v[14:19], v[184:189], v[138:141], v164, v190 op_sel_hi:[0,0,0] cbsz:2 blgp:2
	v_mov_b32_e32 v206, v218
	v_mov_b32_e32 v207, v219
	s_nop 1
	v_mfma_scale_f32_16x16x128_f8f6f4 v[134:137], v[20:25], v[202:207], v[134:137], v168, v220 op_sel_hi:[0,0,0] cbsz:2 blgp:2
	s_nop 1
	v_mfma_scale_f32_16x16x128_f8f6f4 v[122:125], v[14:19], v[202:207], v[122:125], v164, v220 op_sel_hi:[0,0,0] cbsz:2 blgp:2
	v_mov_b32_e32 v212, v222
	v_mov_b32_e32 v213, v223
	s_nop 1
	v_mfma_scale_f32_16x16x128_f8f6f4 v[118:121], v[20:25], v[208:213], v[118:121], v168, v224 op_sel_hi:[0,0,0] cbsz:2 blgp:2
	s_nop 1
	v_mfma_scale_f32_16x16x128_f8f6f4 v[106:109], v[14:19], v[208:213], v[106:109], v164, v224 op_sel_hi:[0,0,0] cbsz:2 blgp:2
	v_mov_b32_e32 v218, v226
	v_mov_b32_e32 v219, v227
	s_nop 1
	v_mfma_scale_f32_16x16x128_f8f6f4 v[102:105], v[20:25], v[214:219], v[102:105], v168, v228 op_sel_hi:[0,0,0] cbsz:2 blgp:2
	s_nop 1
	v_mfma_scale_f32_16x16x128_f8f6f4 v[90:93], v[14:19], v[214:219], v[90:93], v164, v228 op_sel_hi:[0,0,0] cbsz:2 blgp:2
	s_setprio 0
	s_setprio 1
	v_mov_b32_e32 v12, v158
	v_mov_b32_e32 v13, v159
	s_nop 1
	v_mfma_scale_f32_16x16x128_f8f6f4 v[146:149], v[8:13], v[184:189], v[146:149], v160, v190 op_sel_hi:[0,0,0] cbsz:2 blgp:2
	v_mov_b32_e32 v6, v154
	v_mov_b32_e32 v7, v155
	s_nop 1
	v_mfma_scale_f32_16x16x128_f8f6f4 v[142:145], v[2:7], v[184:189], v[142:145], v156, v190 op_sel_hi:[0,0,0] cbsz:2 blgp:2
	s_nop 1
	v_mfma_scale_f32_16x16x128_f8f6f4 v[130:133], v[8:13], v[202:207], v[130:133], v160, v220 op_sel_hi:[0,0,0] cbsz:2 blgp:2
	s_nop 1
	v_mfma_scale_f32_16x16x128_f8f6f4 v[126:129], v[2:7], v[202:207], v[126:129], v156, v220 op_sel_hi:[0,0,0] cbsz:2 blgp:2
	s_nop 1
	v_mfma_scale_f32_16x16x128_f8f6f4 v[114:117], v[8:13], v[208:213], v[114:117], v160, v224 op_sel_hi:[0,0,0] cbsz:2 blgp:2
	s_nop 1
	v_mfma_scale_f32_16x16x128_f8f6f4 v[110:113], v[2:7], v[208:213], v[110:113], v156, v224 op_sel_hi:[0,0,0] cbsz:2 blgp:2
	s_nop 1
	v_mfma_scale_f32_16x16x128_f8f6f4 v[98:101], v[8:13], v[214:219], v[98:101], v160, v228 op_sel_hi:[0,0,0] cbsz:2 blgp:2
	s_nop 1
	v_mfma_scale_f32_16x16x128_f8f6f4 v[94:97], v[2:7], v[214:219], v[94:97], v156, v228 op_sel_hi:[0,0,0] cbsz:2 blgp:2
	s_setprio 0
	s_barrier
	s_add_i32 s62, s42, s35
	v_lshl_add_u64 v[184:185], s[24:25], 0, v[176:177]
	s_mov_b32 m0, s62
	ds_read_b128 v[202:205], v198 offset:16384
	ds_read_b128 v[224:227], v198 offset:17408
	ds_read_b128 v[208:211], v198 offset:18432
	ds_read_b128 v[228:231], v198 offset:19456
	ds_read_b128 v[214:217], v198 offset:20480
	ds_read_b128 v[232:235], v198 offset:21504
	ds_read_b128 v[220:223], v198 offset:22528
	ds_read_b128 v[236:239], v198 offset:23552
	global_load_lds_dwordx4 v176, s[24:25]
	s_add_i32 m0, s62, 0x2000
	s_add_u32 s62, s24, 0x40000
	v_lshl_add_u64 v[186:187], s[24:25], 0, v[172:173]
	s_addc_u32 s63, s25, 0
	s_add_i32 s64, s43, s35
	global_load_lds_dwordx4 v172, s[24:25]
	s_mov_b32 m0, s64
	v_lshl_add_u64 v[188:189], s[26:27], 0, v[178:179]
	global_load_lds_dwordx4 v176, s[62:63]
	s_add_i32 m0, s64, 0x2000
	v_lshl_add_u64 v[190:191], s[26:27], 0, v[174:175]
	global_load_lds_dwordx4 v172, s[62:63]
	s_mov_b32 m0, s21
	s_nop 0
	global_load_lds_dwordx4 v178, s[26:27]
	s_mov_b32 m0, s36
	s_nop 0
	global_load_lds_dwordx4 v174, s[26:27]
	s_waitcnt vmcnt(8)
	s_waitcnt lgkmcnt(0)
	s_barrier
	s_setprio 1
	s_waitcnt lgkmcnt(0)
	v_mov_b32_e32 v206, v224
	v_mov_b32_e32 v207, v225
	s_nop 1
	v_mfma_scale_f32_16x16x128_f8f6f4 v[86:89], v[20:25], v[202:207], v[86:89], v168, v226 op_sel_hi:[0,0,0] cbsz:2 blgp:2
	s_nop 1
	v_mfma_scale_f32_16x16x128_f8f6f4 v[74:77], v[14:19], v[202:207], v[74:77], v164, v226 op_sel_hi:[0,0,0] cbsz:2 blgp:2
	v_mov_b32_e32 v212, v228
	v_mov_b32_e32 v213, v229
	s_nop 1
	v_mfma_scale_f32_16x16x128_f8f6f4 v[70:73], v[20:25], v[208:213], v[70:73], v168, v230 op_sel_hi:[0,0,0] cbsz:2 blgp:2
	s_nop 1
	v_mfma_scale_f32_16x16x128_f8f6f4 v[58:61], v[14:19], v[208:213], v[58:61], v164, v230 op_sel_hi:[0,0,0] cbsz:2 blgp:2
	v_mov_b32_e32 v218, v232
	v_mov_b32_e32 v219, v233
	s_nop 1
	v_mfma_scale_f32_16x16x128_f8f6f4 v[54:57], v[20:25], v[214:219], v[54:57], v168, v234 op_sel_hi:[0,0,0] cbsz:2 blgp:2
	s_nop 1
	v_mfma_scale_f32_16x16x128_f8f6f4 v[42:45], v[14:19], v[214:219], v[42:45], v164, v234 op_sel_hi:[0,0,0] cbsz:2 blgp:2
	v_mov_b32_e32 v224, v236
	v_mov_b32_e32 v225, v237
	s_nop 1
	v_mfma_scale_f32_16x16x128_f8f6f4 v[38:41], v[20:25], v[220:225], v[38:41], v168, v238 op_sel_hi:[0,0,0] cbsz:2 blgp:2
	s_nop 1
	v_mfma_scale_f32_16x16x128_f8f6f4 v[26:29], v[14:19], v[220:225], v[26:29], v164, v238 op_sel_hi:[0,0,0] cbsz:2 blgp:2
	s_setprio 0
	s_setprio 1
	s_nop 1
	v_mfma_scale_f32_16x16x128_f8f6f4 v[82:85], v[8:13], v[202:207], v[82:85], v160, v226 op_sel_hi:[0,0,0] cbsz:2 blgp:2
	s_nop 1
	v_mfma_scale_f32_16x16x128_f8f6f4 v[78:81], v[2:7], v[202:207], v[78:81], v156, v226 op_sel_hi:[0,0,0] cbsz:2 blgp:2
	s_nop 1
	v_mfma_scale_f32_16x16x128_f8f6f4 v[66:69], v[8:13], v[208:213], v[66:69], v160, v230 op_sel_hi:[0,0,0] cbsz:2 blgp:2
	s_nop 1
	v_mfma_scale_f32_16x16x128_f8f6f4 v[62:65], v[2:7], v[208:213], v[62:65], v156, v230 op_sel_hi:[0,0,0] cbsz:2 blgp:2
	s_nop 1
	v_mfma_scale_f32_16x16x128_f8f6f4 v[50:53], v[8:13], v[214:219], v[50:53], v160, v234 op_sel_hi:[0,0,0] cbsz:2 blgp:2
	s_nop 1
	v_mfma_scale_f32_16x16x128_f8f6f4 v[46:49], v[2:7], v[214:219], v[46:49], v156, v234 op_sel_hi:[0,0,0] cbsz:2 blgp:2
	s_nop 1
	v_mfma_scale_f32_16x16x128_f8f6f4 v[34:37], v[8:13], v[220:225], v[34:37], v160, v238 op_sel_hi:[0,0,0] cbsz:2 blgp:2
	s_nop 1
	v_mfma_scale_f32_16x16x128_f8f6f4 v[30:33], v[2:7], v[220:225], v[30:33], v156, v238 op_sel_hi:[0,0,0] cbsz:2 blgp:2
	s_setprio 0
	s_barrier
	s_add_i32 s62, 0, 0x18000
	s_add_i32 s63, 0, 0x1c000
	v_add_u32_e32 v2, s62, v194
	v_add_u32_e32 v6, s63, v194
	ds_read_b128 v[20:23], v2
	ds_read_b128 v[166:169], v2 offset:1024
	ds_read_b128 v[14:17], v2 offset:2048
	ds_read_b128 v[162:165], v2 offset:3072
	ds_read_b128 v[8:11], v6
	ds_read_b128 v[154:157], v6 offset:1024
	ds_read_b128 v[2:5], v6 offset:2048
	ds_read_b128 v[158:161], v6 offset:3072
	s_add_u32 s26, s26, 0x40000
	s_addc_u32 s27, s27, 0
	s_mov_b32 m0, s37
	ds_read_b128 v[202:205], v198 offset:32768
	ds_read_b128 v[224:227], v198 offset:33792
	ds_read_b128 v[208:211], v198 offset:34816
	ds_read_b128 v[228:231], v198 offset:35840
	ds_read_b128 v[214:217], v198 offset:36864
	ds_read_b128 v[232:235], v198 offset:37888
	ds_read_b128 v[220:223], v198 offset:38912
	ds_read_b128 v[236:239], v198 offset:39936
	global_load_lds_dwordx4 v178, s[26:27]
	s_mov_b32 m0, s38
	s_nop 0
	global_load_lds_dwordx4 v174, s[26:27]
	s_waitcnt vmcnt(8)
	s_waitcnt lgkmcnt(0)
	s_barrier
	s_setprio 1
	s_waitcnt lgkmcnt(0)
	v_mov_b32_e32 v24, v166
	v_mov_b32_e32 v25, v167
	v_mov_b32_e32 v206, v224
	v_mov_b32_e32 v207, v225
	s_nop 1
	v_mfma_scale_f32_16x16x128_f8f6f4 v[150:153], v[20:25], v[202:207], v[150:153], v168, v226 op_sel_hi:[0,0,0] cbsz:2 blgp:2
	v_mov_b32_e32 v18, v162
	v_mov_b32_e32 v19, v163
	s_nop 1
	v_mfma_scale_f32_16x16x128_f8f6f4 v[138:141], v[14:19], v[202:207], v[138:141], v164, v226 op_sel_hi:[0,0,0] cbsz:2 blgp:2
	v_mov_b32_e32 v212, v228
	v_mov_b32_e32 v213, v229
	s_nop 1
	v_mfma_scale_f32_16x16x128_f8f6f4 v[134:137], v[20:25], v[208:213], v[134:137], v168, v230 op_sel_hi:[0,0,0] cbsz:2 blgp:2
	s_nop 1
	v_mfma_scale_f32_16x16x128_f8f6f4 v[122:125], v[14:19], v[208:213], v[122:125], v164, v230 op_sel_hi:[0,0,0] cbsz:2 blgp:2
	v_mov_b32_e32 v218, v232
	v_mov_b32_e32 v219, v233
	s_nop 1
	v_mfma_scale_f32_16x16x128_f8f6f4 v[118:121], v[20:25], v[214:219], v[118:121], v168, v234 op_sel_hi:[0,0,0] cbsz:2 blgp:2
	s_nop 1
	v_mfma_scale_f32_16x16x128_f8f6f4 v[106:109], v[14:19], v[214:219], v[106:109], v164, v234 op_sel_hi:[0,0,0] cbsz:2 blgp:2
	v_mov_b32_e32 v224, v236
	v_mov_b32_e32 v225, v237
	s_nop 1
	v_mfma_scale_f32_16x16x128_f8f6f4 v[102:105], v[20:25], v[220:225], v[102:105], v168, v238 op_sel_hi:[0,0,0] cbsz:2 blgp:2
	s_nop 1
	v_mfma_scale_f32_16x16x128_f8f6f4 v[90:93], v[14:19], v[220:225], v[90:93], v164, v238 op_sel_hi:[0,0,0] cbsz:2 blgp:2
	s_setprio 0
	s_setprio 1
	v_mov_b32_e32 v12, v154
	v_mov_b32_e32 v13, v155
	s_nop 1
	v_mfma_scale_f32_16x16x128_f8f6f4 v[146:149], v[8:13], v[202:207], v[146:149], v156, v226 op_sel_hi:[0,0,0] cbsz:2 blgp:2
	v_mov_b32_e32 v6, v158
	v_mov_b32_e32 v7, v159
	s_nop 1
	v_mfma_scale_f32_16x16x128_f8f6f4 v[142:145], v[2:7], v[202:207], v[142:145], v160, v226 op_sel_hi:[0,0,0] cbsz:2 blgp:2
	s_nop 1
	v_mfma_scale_f32_16x16x128_f8f6f4 v[130:133], v[8:13], v[208:213], v[130:133], v156, v230 op_sel_hi:[0,0,0] cbsz:2 blgp:2
	s_nop 1
	v_mfma_scale_f32_16x16x128_f8f6f4 v[126:129], v[2:7], v[208:213], v[126:129], v160, v230 op_sel_hi:[0,0,0] cbsz:2 blgp:2
	s_nop 1
	v_mfma_scale_f32_16x16x128_f8f6f4 v[114:117], v[8:13], v[214:219], v[114:117], v156, v234 op_sel_hi:[0,0,0] cbsz:2 blgp:2
	s_nop 1
	v_mfma_scale_f32_16x16x128_f8f6f4 v[110:113], v[2:7], v[214:219], v[110:113], v160, v234 op_sel_hi:[0,0,0] cbsz:2 blgp:2
	s_nop 1
	v_mfma_scale_f32_16x16x128_f8f6f4 v[98:101], v[8:13], v[220:225], v[98:101], v156, v238 op_sel_hi:[0,0,0] cbsz:2 blgp:2
	s_nop 1
	v_mfma_scale_f32_16x16x128_f8f6f4 v[94:97], v[2:7], v[220:225], v[94:97], v160, v238 op_sel_hi:[0,0,0] cbsz:2 blgp:2
	s_setprio 0
	s_barrier
	s_add_i32 s26, s62, s35
	v_lshl_add_u64 v[154:155], v[184:185], 0, s[6:7]
	s_mov_b32 m0, s26
	ds_read_b128 v[202:205], v198 offset:49152
	ds_read_b128 v[224:227], v198 offset:50176
	ds_read_b128 v[208:211], v198 offset:51200
	ds_read_b128 v[228:231], v198 offset:52224
	ds_read_b128 v[214:217], v198 offset:53248
	ds_read_b128 v[232:235], v198 offset:54272
	ds_read_b128 v[220:223], v198 offset:55296
	ds_read_b128 v[236:239], v198 offset:56320
	global_load_lds_dwordx4 v[154:155], off
	s_add_i32 m0, s26, 0x2000
	s_add_u32 s24, s24, 0x40080
	v_lshl_add_u64 v[154:155], v[186:187], 0, s[6:7]
	s_addc_u32 s25, s25, 0
	s_add_i32 s26, s63, s35
	global_load_lds_dwordx4 v[154:155], off
	s_mov_b32 m0, s26
	s_nop 0
	global_load_lds_dwordx4 v176, s[24:25]
	s_add_i32 m0, s26, 0x2000
	s_nop 0
	global_load_lds_dwordx4 v172, s[24:25]
	v_lshl_add_u64 v[154:155], v[188:189], 0, s[6:7]
	s_mov_b32 m0, s40
	s_nop 0
	global_load_lds_dwordx4 v[154:155], off
	v_lshl_add_u64 v[154:155], v[190:191], 0, s[6:7]
	s_mov_b32 m0, s41
	s_nop 0
	global_load_lds_dwordx4 v[154:155], off
	s_waitcnt vmcnt(8)
	s_waitcnt lgkmcnt(0)
	s_barrier
	s_setprio 1
	s_waitcnt lgkmcnt(0)
	v_mov_b32_e32 v206, v224
	v_mov_b32_e32 v207, v225
	s_nop 1
	v_mfma_scale_f32_16x16x128_f8f6f4 v[86:89], v[20:25], v[202:207], v[86:89], v168, v226 op_sel_hi:[0,0,0] cbsz:2 blgp:2
	s_nop 1
	v_mfma_scale_f32_16x16x128_f8f6f4 v[74:77], v[14:19], v[202:207], v[74:77], v164, v226 op_sel_hi:[0,0,0] cbsz:2 blgp:2
	v_mov_b32_e32 v212, v228
	v_mov_b32_e32 v213, v229
	s_nop 1
	v_mfma_scale_f32_16x16x128_f8f6f4 v[70:73], v[20:25], v[208:213], v[70:73], v168, v230 op_sel_hi:[0,0,0] cbsz:2 blgp:2
	s_nop 1
	v_mfma_scale_f32_16x16x128_f8f6f4 v[58:61], v[14:19], v[208:213], v[58:61], v164, v230 op_sel_hi:[0,0,0] cbsz:2 blgp:2
	v_mov_b32_e32 v218, v232
	v_mov_b32_e32 v219, v233
	s_nop 1
	v_mfma_scale_f32_16x16x128_f8f6f4 v[54:57], v[20:25], v[214:219], v[54:57], v168, v234 op_sel_hi:[0,0,0] cbsz:2 blgp:2
	s_nop 1
	v_mfma_scale_f32_16x16x128_f8f6f4 v[42:45], v[14:19], v[214:219], v[42:45], v164, v234 op_sel_hi:[0,0,0] cbsz:2 blgp:2
	v_mov_b32_e32 v224, v236
	v_mov_b32_e32 v225, v237
	s_nop 1
	v_mfma_scale_f32_16x16x128_f8f6f4 v[38:41], v[20:25], v[220:225], v[38:41], v168, v238 op_sel_hi:[0,0,0] cbsz:2 blgp:2
	s_nop 1
	v_mfma_scale_f32_16x16x128_f8f6f4 v[26:29], v[14:19], v[220:225], v[26:29], v164, v238 op_sel_hi:[0,0,0] cbsz:2 blgp:2
	s_setprio 0
	s_setprio 1
	s_nop 1
	v_mfma_scale_f32_16x16x128_f8f6f4 v[82:85], v[8:13], v[202:207], v[82:85], v156, v226 op_sel_hi:[0,0,0] cbsz:2 blgp:2
	s_nop 1
	v_mfma_scale_f32_16x16x128_f8f6f4 v[78:81], v[2:7], v[202:207], v[78:81], v160, v226 op_sel_hi:[0,0,0] cbsz:2 blgp:2
	s_nop 1
	v_mfma_scale_f32_16x16x128_f8f6f4 v[66:69], v[8:13], v[208:213], v[66:69], v156, v230 op_sel_hi:[0,0,0] cbsz:2 blgp:2
	s_nop 1
	v_mfma_scale_f32_16x16x128_f8f6f4 v[62:65], v[2:7], v[208:213], v[62:65], v160, v230 op_sel_hi:[0,0,0] cbsz:2 blgp:2
	s_nop 1
	v_mfma_scale_f32_16x16x128_f8f6f4 v[50:53], v[8:13], v[214:219], v[50:53], v156, v234 op_sel_hi:[0,0,0] cbsz:2 blgp:2
	s_nop 1
	v_mfma_scale_f32_16x16x128_f8f6f4 v[46:49], v[2:7], v[214:219], v[46:49], v160, v234 op_sel_hi:[0,0,0] cbsz:2 blgp:2
	s_nop 1
	v_mfma_scale_f32_16x16x128_f8f6f4 v[34:37], v[8:13], v[220:225], v[34:37], v156, v238 op_sel_hi:[0,0,0] cbsz:2 blgp:2
	s_nop 1
	v_mfma_scale_f32_16x16x128_f8f6f4 v[30:33], v[2:7], v[220:225], v[30:33], v160, v238 op_sel_hi:[0,0,0] cbsz:2 blgp:2
	s_setprio 0
	s_barrier
	s_add_i32 s61, s61, 2
	s_add_u32 s22, s22, 0x100
	s_addc_u32 s23, s23, 0
	s_add_u32 s51, s51, 0x100
	s_addc_u32 s60, s60, 0
	s_cmp_gt_u32 s61, 13
	s_cbranch_scc0 .LBB0_1279
	s_and_b64 vcc, exec, s[8:9]
	s_cbranch_vccz .LBB0_1282
	s_barrier

.LBB0_1391:
	ds_read_b128 v[24:27], v186
	ds_read_b128 v[28:31], v186 offset:1024
	ds_read_b128 v[16:19], v186 offset:2048
	ds_read_b128 v[20:23], v186 offset:3072
	ds_read_b128 v[8:11], v187
	ds_read_b128 v[12:15], v187 offset:1024
	ds_read_b128 v[0:3], v187 offset:2048
	ds_read_b128 v[4:7], v187 offset:3072
	s_add_u32 s26, s24, 0xfff20080
	s_addc_u32 s27, s25, -1
	s_cmp_eq_u32 s67, 52
	s_cselect_b32 s29, s23, s27
	s_cselect_b32 s28, s22, s26
	s_cselect_b32 s27, s1, s66
	s_cselect_b32 s26, s0, s65
	s_add_i32 m0, s36, 0xc000
	ds_read_b128 v[174:177], v188
	ds_read_b128 v[178:181], v188 offset:1024
	ds_read_b128 v[192:195], v188 offset:2048
	ds_read_b128 v[196:199], v188 offset:3072
	ds_read_b128 v[202:205], v188 offset:4096
	ds_read_b128 v[206:209], v188 offset:5120
	ds_read_b128 v[210:213], v188 offset:6144
	ds_read_b128 v[214:217], v188 offset:7168
	global_load_lds_dwordx4 v170, s[24:25]
	s_add_i32 m0, s36, 0xe000
	s_nop 0
	global_load_lds_dwordx4 v172, s[24:25]
	s_waitcnt vmcnt(8)
	s_waitcnt lgkmcnt(0)
	s_barrier
	s_setprio 1
	s_waitcnt lgkmcnt(0)
	v_mfma_scale_f32_16x16x128_f8f6f4 v[156:159], v[24:31], v[174:181], v[156:159], v189, v190 op_sel_hi:[0,0,0]
	v_mfma_scale_f32_16x16x128_f8f6f4 v[152:155], v[16:23], v[174:181], v[152:155], v189, v190 op_sel_hi:[0,0,0]
	v_mfma_scale_f32_16x16x128_f8f6f4 v[140:143], v[24:31], v[192:199], v[140:143], v189, v190 op_sel_hi:[0,0,0]
	v_mfma_scale_f32_16x16x128_f8f6f4 v[136:139], v[16:23], v[192:199], v[136:139], v189, v190 op_sel_hi:[0,0,0]
	v_mfma_scale_f32_16x16x128_f8f6f4 v[124:127], v[24:31], v[202:209], v[124:127], v189, v190 op_sel_hi:[0,0,0]
	v_mfma_scale_f32_16x16x128_f8f6f4 v[120:123], v[16:23], v[202:209], v[120:123], v189, v190 op_sel_hi:[0,0,0]
	v_mfma_scale_f32_16x16x128_f8f6f4 v[108:111], v[24:31], v[210:217], v[108:111], v189, v190 op_sel_hi:[0,0,0]
	v_mfma_scale_f32_16x16x128_f8f6f4 v[104:107], v[16:23], v[210:217], v[104:107], v189, v190 op_sel_hi:[0,0,0]
	s_setprio 0
	s_setprio 1
	v_mfma_scale_f32_16x16x128_f8f6f4 v[148:151], v[8:15], v[174:181], v[148:151], v189, v190 op_sel_hi:[0,0,0]
	v_mfma_scale_f32_16x16x128_f8f6f4 v[144:147], v[0:7], v[174:181], v[144:147], v189, v190 op_sel_hi:[0,0,0]
	v_mfma_scale_f32_16x16x128_f8f6f4 v[132:135], v[8:15], v[192:199], v[132:135], v189, v190 op_sel_hi:[0,0,0]
	v_mfma_scale_f32_16x16x128_f8f6f4 v[128:131], v[0:7], v[192:199], v[128:131], v189, v190 op_sel_hi:[0,0,0]
	v_mfma_scale_f32_16x16x128_f8f6f4 v[116:119], v[8:15], v[202:209], v[116:119], v189, v190 op_sel_hi:[0,0,0]
	v_mfma_scale_f32_16x16x128_f8f6f4 v[112:115], v[0:7], v[202:209], v[112:115], v189, v190 op_sel_hi:[0,0,0]
	v_mfma_scale_f32_16x16x128_f8f6f4 v[100:103], v[8:15], v[210:217], v[100:103], v189, v190 op_sel_hi:[0,0,0]
	v_mfma_scale_f32_16x16x128_f8f6f4 v[96:99], v[0:7], v[210:217], v[96:99], v189, v190 op_sel_hi:[0,0,0]
	s_setprio 0
	s_barrier
	s_add_i32 s68, s44, s35
	v_lshl_add_u64 v[174:175], s[26:27], 0, v[160:161]
	s_mov_b32 m0, s68
	ds_read_b128 v[192:195], v188 offset:16384
	ds_read_b128 v[196:199], v188 offset:17408
	ds_read_b128 v[202:205], v188 offset:18432
	ds_read_b128 v[206:209], v188 offset:19456
	ds_read_b128 v[210:213], v188 offset:20480
	ds_read_b128 v[214:217], v188 offset:21504
	ds_read_b128 v[218:221], v188 offset:22528
	ds_read_b128 v[222:225], v188 offset:23552
	global_load_lds_dwordx4 v160, s[26:27]
	s_add_i32 m0, s68, 0x2000
	s_add_u32 s68, s26, 0xe0000
	v_lshl_add_u64 v[176:177], s[26:27], 0, v[164:165]
	s_addc_u32 s69, s27, 0
	s_add_i32 s70, s45, s35
	global_load_lds_dwordx4 v164, s[26:27]
	s_mov_b32 m0, s70
	v_lshl_add_u64 v[180:181], s[28:29], 0, v[166:167]
	global_load_lds_dwordx4 v160, s[68:69]
	s_add_i32 m0, s70, 0x2000
	s_nop 0
	global_load_lds_dwordx4 v164, s[68:69]
	v_lshl_add_u64 v[178:179], s[28:29], 0, v[168:169]
	s_mov_b32 m0, s36
	s_nop 0
	global_load_lds_dwordx4 v168, s[28:29]
	s_mov_b32 m0, s37
	s_nop 0
	global_load_lds_dwordx4 v166, s[28:29]
	s_waitcnt vmcnt(8)
	s_waitcnt lgkmcnt(0)
	s_barrier
	s_setprio 1
	s_waitcnt lgkmcnt(0)
	v_mfma_scale_f32_16x16x128_f8f6f4 v[92:95], v[24:31], v[192:199], v[92:95], v189, v190 op_sel_hi:[0,0,0]
	v_mfma_scale_f32_16x16x128_f8f6f4 v[88:91], v[16:23], v[192:199], v[88:91], v189, v190 op_sel_hi:[0,0,0]
	v_mfma_scale_f32_16x16x128_f8f6f4 v[76:79], v[24:31], v[202:209], v[76:79], v189, v190 op_sel_hi:[0,0,0]
	v_mfma_scale_f32_16x16x128_f8f6f4 v[72:75], v[16:23], v[202:209], v[72:75], v189, v190 op_sel_hi:[0,0,0]
	v_mfma_scale_f32_16x16x128_f8f6f4 v[60:63], v[24:31], v[210:217], v[60:63], v189, v190 op_sel_hi:[0,0,0]
	v_mfma_scale_f32_16x16x128_f8f6f4 v[56:59], v[16:23], v[210:217], v[56:59], v189, v190 op_sel_hi:[0,0,0]
	v_mfma_scale_f32_16x16x128_f8f6f4 v[44:47], v[24:31], v[218:225], v[44:47], v189, v190 op_sel_hi:[0,0,0]
	v_mfma_scale_f32_16x16x128_f8f6f4 v[40:43], v[16:23], v[218:225], v[40:43], v189, v190 op_sel_hi:[0,0,0]
	s_setprio 0
	s_setprio 1
	v_mfma_scale_f32_16x16x128_f8f6f4 v[84:87], v[8:15], v[192:199], v[84:87], v189, v190 op_sel_hi:[0,0,0]
	v_mfma_scale_f32_16x16x128_f8f6f4 v[80:83], v[0:7], v[192:199], v[80:83], v189, v190 op_sel_hi:[0,0,0]
	v_mfma_scale_f32_16x16x128_f8f6f4 v[68:71], v[8:15], v[202:209], v[68:71], v189, v190 op_sel_hi:[0,0,0]
	v_mfma_scale_f32_16x16x128_f8f6f4 v[64:67], v[0:7], v[202:209], v[64:67], v189, v190 op_sel_hi:[0,0,0]
	v_mfma_scale_f32_16x16x128_f8f6f4 v[52:55], v[8:15], v[210:217], v[52:55], v189, v190 op_sel_hi:[0,0,0]
	v_mfma_scale_f32_16x16x128_f8f6f4 v[48:51], v[0:7], v[210:217], v[48:51], v189, v190 op_sel_hi:[0,0,0]
	v_mfma_scale_f32_16x16x128_f8f6f4 v[36:39], v[8:15], v[218:225], v[36:39], v189, v190 op_sel_hi:[0,0,0]
	v_mfma_scale_f32_16x16x128_f8f6f4 v[32:35], v[0:7], v[218:225], v[32:35], v189, v190 op_sel_hi:[0,0,0]
	s_setprio 0
	s_barrier
	s_add_i32 s68, 0, 0x18000
	s_add_i32 s69, 0, 0x1c000
	v_add_u32_e32 v12, s68, v184
	v_add_u32_e32 v28, s69, v184
	ds_read_b128 v[0:3], v12
	ds_read_b128 v[4:7], v12 offset:1024
	ds_read_b128 v[8:11], v12 offset:2048
	ds_read_b128 v[12:15], v12 offset:3072
	ds_read_b128 v[16:19], v28
	ds_read_b128 v[20:23], v28 offset:1024
	ds_read_b128 v[24:27], v28 offset:2048
	ds_read_b128 v[28:31], v28 offset:3072
	s_add_u32 s28, s28, 0xe0000
	s_addc_u32 s29, s29, 0
	s_mov_b32 m0, s38
	ds_read_b128 v[192:195], v188 offset:32768
	ds_read_b128 v[196:199], v188 offset:33792
	ds_read_b128 v[202:205], v188 offset:34816
	ds_read_b128 v[206:209], v188 offset:35840
	ds_read_b128 v[210:213], v188 offset:36864
	ds_read_b128 v[214:217], v188 offset:37888
	ds_read_b128 v[218:221], v188 offset:38912
	ds_read_b128 v[222:225], v188 offset:39936
	global_load_lds_dwordx4 v168, s[28:29]
	s_mov_b32 m0, s39
	s_nop 0
	global_load_lds_dwordx4 v166, s[28:29]
	s_waitcnt vmcnt(8)
	s_waitcnt lgkmcnt(0)
	s_barrier
	s_setprio 1
	s_waitcnt lgkmcnt(0)
	v_mfma_scale_f32_16x16x128_f8f6f4 v[156:159], v[0:7], v[192:199], v[156:159], v189, v190 op_sel_hi:[0,0,0]
	v_mfma_scale_f32_16x16x128_f8f6f4 v[152:155], v[8:15], v[192:199], v[152:155], v189, v190 op_sel_hi:[0,0,0]
	v_mfma_scale_f32_16x16x128_f8f6f4 v[140:143], v[0:7], v[202:209], v[140:143], v189, v190 op_sel_hi:[0,0,0]
	v_mfma_scale_f32_16x16x128_f8f6f4 v[136:139], v[8:15], v[202:209], v[136:139], v189, v190 op_sel_hi:[0,0,0]
	v_mfma_scale_f32_16x16x128_f8f6f4 v[124:127], v[0:7], v[210:217], v[124:127], v189, v190 op_sel_hi:[0,0,0]
	v_mfma_scale_f32_16x16x128_f8f6f4 v[120:123], v[8:15], v[210:217], v[120:123], v189, v190 op_sel_hi:[0,0,0]
	v_mfma_scale_f32_16x16x128_f8f6f4 v[108:111], v[0:7], v[218:225], v[108:111], v189, v190 op_sel_hi:[0,0,0]
	v_mfma_scale_f32_16x16x128_f8f6f4 v[104:107], v[8:15], v[218:225], v[104:107], v189, v190 op_sel_hi:[0,0,0]
	s_setprio 0
	s_setprio 1
	v_mfma_scale_f32_16x16x128_f8f6f4 v[148:151], v[16:23], v[192:199], v[148:151], v189, v190 op_sel_hi:[0,0,0]
	v_mfma_scale_f32_16x16x128_f8f6f4 v[144:147], v[24:31], v[192:199], v[144:147], v189, v190 op_sel_hi:[0,0,0]
	v_mfma_scale_f32_16x16x128_f8f6f4 v[132:135], v[16:23], v[202:209], v[132:135], v189, v190 op_sel_hi:[0,0,0]
	v_mfma_scale_f32_16x16x128_f8f6f4 v[128:131], v[24:31], v[202:209], v[128:131], v189, v190 op_sel_hi:[0,0,0]
	v_mfma_scale_f32_16x16x128_f8f6f4 v[116:119], v[16:23], v[210:217], v[116:119], v189, v190 op_sel_hi:[0,0,0]
	v_mfma_scale_f32_16x16x128_f8f6f4 v[112:115], v[24:31], v[210:217], v[112:115], v189, v190 op_sel_hi:[0,0,0]
	v_mfma_scale_f32_16x16x128_f8f6f4 v[100:103], v[16:23], v[218:225], v[100:103], v189, v190 op_sel_hi:[0,0,0]
	v_mfma_scale_f32_16x16x128_f8f6f4 v[96:99], v[24:31], v[218:225], v[96:99], v189, v190 op_sel_hi:[0,0,0]
	s_setprio 0
	s_barrier
	s_add_i32 s28, s68, s35
	v_lshl_add_u64 v[174:175], v[174:175], 0, s[8:9]
	s_mov_b32 m0, s28
	ds_read_b128 v[192:195], v188 offset:49152
	ds_read_b128 v[196:199], v188 offset:50176
	ds_read_b128 v[202:205], v188 offset:51200
	ds_read_b128 v[206:209], v188 offset:52224
	ds_read_b128 v[210:213], v188 offset:53248
	ds_read_b128 v[214:217], v188 offset:54272
	ds_read_b128 v[218:221], v188 offset:55296
	ds_read_b128 v[222:225], v188 offset:56320
	global_load_lds_dwordx4 v[174:175], off
	s_add_i32 m0, s28, 0x2000
	s_add_u32 s26, s26, 0xe0080
	v_lshl_add_u64 v[174:175], v[176:177], 0, s[8:9]
	s_addc_u32 s27, s27, 0
	s_add_i32 s28, s69, s35
	global_load_lds_dwordx4 v[174:175], off
	s_mov_b32 m0, s28
	s_nop 0
	global_load_lds_dwordx4 v160, s[26:27]
	s_add_i32 m0, s28, 0x2000
	s_nop 0
	global_load_lds_dwordx4 v164, s[26:27]
	v_lshl_add_u64 v[174:175], v[178:179], 0, s[8:9]
	s_mov_b32 m0, s41
	s_nop 0
	global_load_lds_dwordx4 v[174:175], off
	v_lshl_add_u64 v[174:175], v[180:181], 0, s[8:9]
	s_mov_b32 m0, s42
	s_nop 0
	global_load_lds_dwordx4 v[174:175], off
	s_waitcnt vmcnt(8)
	s_waitcnt lgkmcnt(0)
	s_barrier
	s_setprio 1
	s_waitcnt lgkmcnt(0)
	v_mfma_scale_f32_16x16x128_f8f6f4 v[92:95], v[0:7], v[192:199], v[92:95], v189, v190 op_sel_hi:[0,0,0]
	v_mfma_scale_f32_16x16x128_f8f6f4 v[88:91], v[8:15], v[192:199], v[88:91], v189, v190 op_sel_hi:[0,0,0]
	v_mfma_scale_f32_16x16x128_f8f6f4 v[76:79], v[0:7], v[202:209], v[76:79], v189, v190 op_sel_hi:[0,0,0]
	v_mfma_scale_f32_16x16x128_f8f6f4 v[72:75], v[8:15], v[202:209], v[72:75], v189, v190 op_sel_hi:[0,0,0]
	v_mfma_scale_f32_16x16x128_f8f6f4 v[60:63], v[0:7], v[210:217], v[60:63], v189, v190 op_sel_hi:[0,0,0]
	v_mfma_scale_f32_16x16x128_f8f6f4 v[56:59], v[8:15], v[210:217], v[56:59], v189, v190 op_sel_hi:[0,0,0]
	v_mfma_scale_f32_16x16x128_f8f6f4 v[44:47], v[0:7], v[218:225], v[44:47], v189, v190 op_sel_hi:[0,0,0]
	v_mfma_scale_f32_16x16x128_f8f6f4 v[40:43], v[8:15], v[218:225], v[40:43], v189, v190 op_sel_hi:[0,0,0]
	s_setprio 0
	s_setprio 1
	v_mfma_scale_f32_16x16x128_f8f6f4 v[84:87], v[16:23], v[192:199], v[84:87], v189, v190 op_sel_hi:[0,0,0]
	v_mfma_scale_f32_16x16x128_f8f6f4 v[80:83], v[24:31], v[192:199], v[80:83], v189, v190 op_sel_hi:[0,0,0]
	v_mfma_scale_f32_16x16x128_f8f6f4 v[68:71], v[16:23], v[202:209], v[68:71], v189, v190 op_sel_hi:[0,0,0]
	v_mfma_scale_f32_16x16x128_f8f6f4 v[64:67], v[24:31], v[202:209], v[64:67], v189, v190 op_sel_hi:[0,0,0]
	v_mfma_scale_f32_16x16x128_f8f6f4 v[52:55], v[16:23], v[210:217], v[52:55], v189, v190 op_sel_hi:[0,0,0]
	v_mfma_scale_f32_16x16x128_f8f6f4 v[48:51], v[24:31], v[210:217], v[48:51], v189, v190 op_sel_hi:[0,0,0]
	v_mfma_scale_f32_16x16x128_f8f6f4 v[36:39], v[16:23], v[218:225], v[36:39], v189, v190 op_sel_hi:[0,0,0]
	v_mfma_scale_f32_16x16x128_f8f6f4 v[32:35], v[24:31], v[218:225], v[32:35], v189, v190 op_sel_hi:[0,0,0]
	s_setprio 0
	s_barrier
	s_add_i32 s67, s67, 2
	s_add_u32 s24, s24, 0x100
	s_addc_u32 s25, s25, 0
	s_add_u32 s65, s65, 0x100
	s_addc_u32 s66, s66, 0
	s_cmp_gt_u32 s67, 53
	s_cbranch_scc0 .LBB0_1391
	s_and_b64 vcc, exec, s[10:11]
	s_cbranch_vccz .LBB0_1394
	s_barrier
